# scan b/k image stored transposed so each recurrence lane reads its four b values with one ds_read_b128; w3 load moved beside the other weight loads, one wait fewer (42 instead of 45 instructions per p
# baseline (speedup 1.0000x reference)
.LBB0_779:
	s_or_b64 exec, exec, s[0:1]
	v_lshlrev_b64 v[2:3], 11, v[126:127]
	v_lshl_add_u64 v[4:5], s[66:67], 0, v[2:3]
	v_lshlrev_b64 v[6:7], 1, v[0:1]
	v_lshl_add_u64 v[4:5], v[4:5], 0, v[6:7]
	global_load_dwordx4 v[40:43], v[4:5], off nt
	v_lshlrev_b64 v[4:5], 12, v[126:127]
	v_lshl_add_u64 v[2:3], s[68:69], 0, v[2:3]
	v_lshl_add_u64 v[4:5], s[64:65], 0, v[4:5]
	s_waitcnt vmcnt(3)
	v_and_b32_e32 v15, 0xffff0000, v16
	v_lshlrev_b32_e32 v60, 16, v17
	v_and_b32_e32 v61, 0xffff0000, v17
	s_waitcnt vmcnt(2)
	v_lshlrev_b32_e32 v62, 16, v20
	v_and_b32_e32 v63, 0xffff0000, v20
	v_lshlrev_b32_e32 v68, 16, v21
	v_and_b32_e32 v69, 0xffff0000, v21
	v_and_b32_e32 v10, 0xffff0000, v28
	v_lshlrev_b32_e32 v11, 16, v29
	v_and_b32_e32 v12, 0xffff0000, v29
	v_lshlrev_b32_e32 v13, 16, v32
	v_and_b32_e32 v44, 0xffff0000, v32
	v_lshlrev_b32_e32 v45, 16, v33
	v_and_b32_e32 v46, 0xffff0000, v33
	v_mov_b32_e32 v48, v124
	v_add_u32_e32 v49, s3, v115
	s_add_i32 s0, 0, 0x20c00
	s_add_i32 s1, 0, 0x20d00
	v_lshl_add_u64 v[2:3], v[2:3], 0, v[6:7]
	v_lshl_add_u64 v[0:1], v[0:1], 2, v[4:5]
	v_lshlrev_b32_e32 v14, 16, v16
	v_lshlrev_b32_e32 v9, 16, v28
	s_add_i32 s2, 0, 0x20e00
	v_add_u32_e32 v50, s0, v115
	v_add_u32_e32 v51, s1, v115
	v_sub_f32_e32 v75, v10, v15
	v_sub_f32_e32 v77, v12, v61
	v_sub_f32_e32 v76, v11, v60
	v_sub_f32_e32 v83, v44, v63
	v_sub_f32_e32 v82, v13, v62
	v_sub_f32_e32 v87, v46, v69
	v_sub_f32_e32 v86, v45, v68
	global_load_dwordx4 v[44:47], v[2:3], off nt
	global_load_dwordx4 v[4:7], v[0:1], off offset:16 nt
	s_nop 0
	global_load_dwordx4 v[0:3], v[0:1], off nt
	ds_read_b128 v[10:13], v49
	v_sub_f32_e32 v74, v9, v14
	v_add_u32_e32 v9, s2, v115
	ds_read_b128 v[52:55], v50
	ds_read_b128 v[48:51], v51
	ds_read_b128 v[56:59], v9
	v_or_b32_e32 v120, 16, v115
	v_add_u32_e32 v103, s3, v120
	s_waitcnt lgkmcnt(3)
	v_pk_fma_f32 v[80:81], v[10:11], v[74:75], v[14:15]
	s_waitcnt lgkmcnt(2)
	v_pk_fma_f32 v[14:15], v[86:87], v[54:55], v[68:69]
	v_pk_fma_f32 v[68:69], v[82:83], v[52:53], v[62:63]
	v_add_u32_e32 v104, s0, v120
	v_pk_fma_f32 v[78:79], v[12:13], v[76:77], v[60:61]
	s_waitcnt lgkmcnt(0)
	v_pk_mul_f32 v[74:75], v[14:15], v[58:59]
	v_pk_mul_f32 v[76:77], v[68:69], v[56:57]
	ds_read_b128 v[52:55], v103
	ds_read_b128 v[56:59], v104
	v_add_u32_e32 v9, s1, v120
	v_add_u32_e32 v60, s2, v120
	ds_read_b128 v[10:13], v9
	ds_read_b128 v[60:63], v60
	v_lshlrev_b32_e32 v70, 16, v22
	v_and_b32_e32 v71, 0xffff0000, v22
	v_lshlrev_b32_e32 v96, 16, v34
	v_and_b32_e32 v97, 0xffff0000, v34
	v_lshlrev_b32_e32 v72, 16, v23
	v_and_b32_e32 v73, 0xffff0000, v23
	v_lshlrev_b32_e32 v98, 16, v35
	v_and_b32_e32 v99, 0xffff0000, v35
	v_sub_f32_e32 v83, v97, v71
	v_sub_f32_e32 v82, v96, v70
	v_sub_f32_e32 v87, v99, v73
	v_sub_f32_e32 v86, v98, v72
	s_waitcnt lgkmcnt(2)
	v_pk_fma_f32 v[56:57], v[82:83], v[56:57], v[70:71]
	v_pk_fma_f32 v[58:59], v[86:87], v[58:59], v[72:73]
	s_waitcnt lgkmcnt(0)
	v_pk_mul_f32 v[98:99], v[56:57], v[60:61]
	v_pk_mul_f32 v[96:97], v[58:59], v[62:63]
	v_mov_b32_e32 v62, v77
	v_mov_b32_e32 v63, v99
	v_mov_b32_e32 v60, v76
	v_mov_b32_e32 v61, v98
	v_pk_mul_f32 v[62:63], v[62:63], v[62:63]
	v_mov_b32_e32 v70, v75
	v_mov_b32_e32 v71, v97
	v_pk_fma_f32 v[60:61], v[60:61], v[60:61], v[62:63]
	v_mov_b32_e32 v62, v74
	v_mov_b32_e32 v63, v96
	v_pk_mul_f32 v[70:71], v[70:71], v[70:71]
	s_mov_b32 s0, 0xf800000
	v_pk_fma_f32 v[62:63], v[62:63], v[62:63], v[70:71]
	v_lshlrev_b32_e32 v64, 16, v18
	v_pk_add_f32 v[60:61], v[60:61], v[62:63]
	v_and_b32_e32 v65, 0xffff0000, v18
	v_add_f32_e32 v9, v60, v61
	v_lshlrev_b32_e32 v84, 16, v30
	v_and_b32_e32 v100, 0xffff0000, v30
	v_add_f32_dpp v9, v9, v9 row_half_mirror row_mask:0xf bank_mask:0xf bound_ctrl:1
	v_sub_f32_e32 v61, v100, v65
	v_lshlrev_b32_e32 v66, 16, v19
	v_add_f32_dpp v9, v9, v9 quad_perm:[3,2,1,0] row_mask:0xf bank_mask:0xf bound_ctrl:1
	v_and_b32_e32 v67, 0xffff0000, v19
	v_lshlrev_b32_e32 v101, 16, v31
	v_add_f32_dpp v9, v9, v9 quad_perm:[1,0,3,2] row_mask:0xf bank_mask:0xf bound_ctrl:1
	v_mul_f32_e32 v60, 0x4f800000, v9
	v_cmp_gt_f32_e32 vcc, s0, v9
	v_and_b32_e32 v102, 0xffff0000, v31
	v_sub_f32_e32 v63, v102, v67
	v_cndmask_b32_e32 v9, v9, v60, vcc
	v_sqrt_f32_e32 v62, v9
	v_sub_f32_e32 v60, v84, v64
	v_pk_fma_f32 v[72:73], v[60:61], v[52:53], v[64:65]
	s_waitcnt vmcnt(3)
	v_lshlrev_b32_e32 v88, 16, v40
	v_add_u32_e32 v70, -1, v62
	v_fma_f32 v71, -v70, v62, v9
	v_cmp_ge_f32_e64 s[0:1], 0, v71
	v_add_u32_e32 v71, 1, v62
	v_and_b32_e32 v89, 0xffff0000, v40
	v_cndmask_b32_e64 v70, v62, v70, s[0:1]
	v_fma_f32 v62, -v71, v62, v9
	v_cmp_lt_f32_e64 s[0:1], 0, v62
	v_lshlrev_b32_e32 v90, 16, v41
	v_and_b32_e32 v91, 0xffff0000, v41
	v_cndmask_b32_e64 v62, v70, v71, s[0:1]
	v_mul_f32_e32 v70, 0x37800000, v62
	v_cndmask_b32_e32 v62, v62, v70, vcc
	v_mov_b32_e32 v70, 0x260
	v_cmp_class_f32_e32 vcc, v9, v70
	v_pk_add_f32 v[60:61], v[88:89], -1.0 op_sel_hi:[1,0]
	v_lshlrev_b32_e32 v92, 16, v42
	v_cndmask_b32_e32 v9, v62, v9, vcc
	v_max_f32_e32 v9, 0x2b8cbccc, v9
	v_div_scale_f32 v82, s[0:1], v9, v9, 1.0
	v_rcp_f32_e32 v83, v82
	v_sub_f32_e32 v62, v101, v66
	v_pk_fma_f32 v[70:71], v[62:63], v[54:55], v[66:67]
	s_add_i32 s0, 0, 0x20f00
	v_fma_f32 v52, -v82, v83, 1.0
	v_fmac_f32_e32 v83, v52, v83
	v_div_scale_f32 v52, vcc, 1.0, v9, 1.0
	v_mul_f32_e32 v53, v52, v83
	v_fma_f32 v54, -v82, v53, v52
	v_fmac_f32_e32 v53, v54, v83
	v_fma_f32 v52, -v82, v53, v52
	v_div_fmas_f32 v52, v52, v83, v53
	v_div_fixup_f32 v84, v52, v9, 1.0
	v_add_u32_e32 v9, s0, v115
	ds_read_b128 v[52:55], v9
	s_add_i32 s1, 0, 0x21000
	v_pk_add_f32 v[62:63], v[90:91], -1.0 op_sel_hi:[1,0]
	v_add_u32_e32 v9, s1, v115
	v_pk_mul_f32 v[82:83], v[76:77], v[84:85] op_sel_hi:[1,0]
	v_pk_mul_f32 v[86:87], v[74:75], v[84:85] op_sel_hi:[1,0]
	ds_read_b128 v[74:77], v9
	s_waitcnt lgkmcnt(1)
	v_pk_fma_f32 v[54:55], v[62:63], v[54:55], 1.0 op_sel_hi:[1,1,0]
	v_pk_fma_f32 v[52:53], v[60:61], v[52:53], 1.0 op_sel_hi:[1,1,0]
	v_add_u32_e32 v9, s0, v120
	v_pk_mul_f32 v[62:63], v[14:15], v[54:55]
	v_pk_mul_f32 v[60:61], v[68:69], v[52:53]
	ds_read_b128 v[52:55], v9
	v_and_b32_e32 v93, 0xffff0000, v42
	v_lshlrev_b32_e32 v94, 16, v43
	v_and_b32_e32 v95, 0xffff0000, v43
	v_pk_mul_f32 v[68:69], v[96:97], v[84:85] op_sel_hi:[1,0]
	v_pk_add_f32 v[96:97], v[92:93], -1.0 op_sel_hi:[1,0]
	v_pk_mul_f32 v[14:15], v[98:99], v[84:85] op_sel_hi:[1,0]
	v_pk_add_f32 v[98:99], v[94:95], -1.0 op_sel_hi:[1,0]
	s_waitcnt lgkmcnt(0)
	v_pk_fma_f32 v[52:53], v[96:97], v[52:53], 1.0 op_sel_hi:[1,1,0]
	v_pk_mul_f32 v[64:65], v[82:83], v[88:89]
	v_pk_fma_f32 v[54:55], v[98:99], v[54:55], 1.0 op_sel_hi:[1,1,0]
	v_pk_mul_f32 v[52:53], v[56:57], v[52:53]
	v_pk_mul_f32 v[56:57], v[14:15], v[92:93]
	v_pk_mul_f32 v[66:67], v[86:87], v[90:91]
	v_pk_mul_f32 v[54:55], v[58:59], v[54:55]
	v_pk_mul_f32 v[58:59], v[68:69], v[94:95]
	v_mov_b32_e32 v96, v73
	v_mov_b32_e32 v97, v81
	v_mov_b32_e32 v98, v57
	v_mov_b32_e32 v99, v65
	v_mov_b32_e32 v92, v72
	v_mov_b32_e32 v93, v80
	v_mov_b32_e32 v94, v56
	v_mov_b32_e32 v95, v64
	v_pk_mul_f32 v[96:97], v[96:97], v[98:99]
	v_mov_b32_e32 v98, v71
	v_mov_b32_e32 v99, v79
	v_mov_b32_e32 v104, v59
	v_mov_b32_e32 v105, v67
	v_pk_mul_f32 v[102:103], v[80:81], v[60:61]
	v_add_u32_e32 v9, s1, v120
	v_pk_fma_f32 v[92:93], v[92:93], v[94:95], v[96:97]
	v_mov_b32_e32 v94, v70
	v_mov_b32_e32 v95, v78
	v_mov_b32_e32 v96, v58
	v_mov_b32_e32 v97, v66
	v_pk_mul_f32 v[98:99], v[98:99], v[104:105]
	ds_read_b128 v[88:91], v9
	v_pk_fma_f32 v[94:95], v[94:95], v[96:97], v[98:99]
	v_mov_b32_e32 v97, v74
	v_mov_b32_e32 v99, v102
	v_mov_b32_e32 v74, v81
	v_mov_b32_e32 v102, v61
	v_pk_mul_f32 v[100:101], v[78:79], v[62:63]
	v_mov_b32_e32 v96, v80
	v_mov_b32_e32 v98, v60
	v_pk_mul_f32 v[74:75], v[74:75], v[102:103]
	v_pk_add_f32 v[92:93], v[92:93], v[94:95]
	v_pk_fma_f32 v[74:75], v[96:97], v[98:99], v[74:75]
	v_mov_b32_e32 v97, v76
	v_mov_b32_e32 v99, v100
	v_mov_b32_e32 v76, v79
	v_mov_b32_e32 v100, v63
	v_mov_b32_e32 v96, v78
	v_mov_b32_e32 v98, v62
	v_pk_mul_f32 v[76:77], v[76:77], v[100:101]
	v_pk_mul_f32 v[94:95], v[72:73], v[52:53]
	v_pk_fma_f32 v[76:77], v[96:97], v[98:99], v[76:77]
	v_add_f32_e32 v9, 0, v93
	v_pk_add_f32 v[74:75], v[74:75], v[76:77]
	s_waitcnt lgkmcnt(0)
	v_mov_b32_e32 v77, v88
	v_mov_b32_e32 v97, v94
	v_mov_b32_e32 v88, v73
	v_mov_b32_e32 v94, v53
	v_add_f32_e32 v9, v92, v9
	v_pk_mul_f32 v[92:93], v[70:71], v[54:55]
	v_mov_b32_e32 v76, v72
	v_mov_b32_e32 v96, v52
	v_pk_mul_f32 v[88:89], v[88:89], v[94:95]
	v_mov_b32_e32 v95, v92
	v_pk_fma_f32 v[76:77], v[76:77], v[96:97], v[88:89]
	v_mov_b32_e32 v89, v90
	v_mov_b32_e32 v90, v71
	v_mov_b32_e32 v92, v55
	v_mov_b32_e32 v88, v70
	v_mov_b32_e32 v94, v54
	v_pk_mul_f32 v[90:91], v[90:91], v[92:93]
	v_add_f32_dpp v9, v9, v9 row_half_mirror row_mask:0xf bank_mask:0xf bound_ctrl:1
	v_pk_fma_f32 v[88:89], v[88:89], v[94:95], v[90:91]
	v_lshlrev_b32_e32 v117, 9, v113
	v_add_f32_dpp v9, v9, v9 quad_perm:[3,2,1,0] row_mask:0xf bank_mask:0xf bound_ctrl:1
	v_pk_add_f32 v[76:77], v[76:77], v[88:89]
	v_and_b32_e32 v88, 8, v112
	v_add_f32_dpp v84, v9, v9 quad_perm:[1,0,3,2] row_mask:0xf bank_mask:0xf bound_ctrl:1
	v_and_or_b32 v116, v85, 64, v88
	v_and_b32_e32 v88, 8, v109
	v_pk_add_f32 v[74:75], v[74:75], 0 op_sel_hi:[1,0]
	v_mov_b32_e32 v85, v84
	v_cmp_ne_u32_e32 vcc, 0, v88
	v_add_u32_e32 v88, 0, v117
	v_lshlrev_b32_e32 v118, 8, v113
	v_mov_b32_e32 v104, 0
	v_mov_b32_e32 v105, 0
	v_mov_b32_e32 v106, v8
	v_mov_b32_e32 v107, v8
	v_pk_add_f32 v[74:75], v[74:75], v[76:77]
	v_mov_b32_e32 v76, v8
	v_mov_b32_e32 v77, v8
	v_sub_u32_e32 v122, v88, v118
	s_movk_i32 s0, 0x300
	v_pk_mul_f32 v[98:99], v[82:83], v[84:85] op_sel_hi:[1,0]
	v_pk_mul_f32 v[96:97], v[86:87], v[84:85] op_sel_hi:[1,0]
	s_waitcnt vmcnt(0)
	v_mov_b32_dpp v104, v0 row_shr:8 row_mask:0xf bank_mask:0xf
	v_mov_b32_dpp v105, v1 row_shr:8 row_mask:0xf bank_mask:0xf
	v_mov_b32_dpp v106, v2 row_shr:8 row_mask:0xf bank_mask:0xf
	v_mov_b32_dpp v107, v3 row_shr:8 row_mask:0xf bank_mask:0xf
	v_mov_b32_dpp v76, v74 row_half_mirror row_mask:0xf bank_mask:0xf
	v_mov_b32_dpp v77, v75 row_half_mirror row_mask:0xf bank_mask:0xf
	v_mad_u32_u24 v123, v113, s0, v122
	v_xor_b32_e32 v102, 0x80000000, v82
	v_xor_b32_e32 v103, 0x80000000, v83
	v_xor_b32_e32 v100, 0x80000000, v86
	v_xor_b32_e32 v101, 0x80000000, v87
	v_pk_fma_f32 v[96:97], v[2:3], v[78:79], v[96:97] neg_lo:[0,0,1] neg_hi:[0,0,1]
	v_pk_fma_f32 v[98:99], v[0:1], v[80:81], v[98:99] neg_lo:[0,0,1] neg_hi:[0,0,1]
	v_pk_mul_f32 v[78:79], v[82:83], v[104:105] neg_lo:[1,0] neg_hi:[1,0]
	v_pk_mul_f32 v[80:81], v[86:87], v[106:107] neg_lo:[1,0] neg_hi:[1,0]
	v_cmp_eq_u32_e64 s[0:1], 0, v114
	v_pk_add_f32 v[74:75], v[74:75], v[76:77]
	v_mov_b32_e32 v76, v8
	v_mov_b32_e32 v77, v8
	v_lshlrev_b32_e32 v119, 8, v114
	v_cndmask_b32_e64 v86, v81, v101, s[0:1]
	v_cndmask_b32_e64 v87, v80, v100, s[0:1]
	v_cndmask_b32_e64 v129, v79, v103, s[0:1]
	v_cndmask_b32_e64 v130, v78, v102, s[0:1]
	v_pk_mul_f32 v[78:79], v[98:99], v[104:105]
	v_pk_mul_f32 v[80:81], v[96:97], v[106:107]
	v_mov_b32_dpp v76, v74 quad_perm:[3,2,1,0] row_mask:0xf bank_mask:0xf
	v_mov_b32_dpp v77, v75 quad_perm:[3,2,1,0] row_mask:0xf bank_mask:0xf
	v_add_u32_e32 v121, v88, v119
	v_and_or_b32 v128, v115, 32, v116
	v_cndmask_b32_e64 v81, v81, v97, s[0:1]
	v_cndmask_b32_e64 v131, v80, v96, s[0:1]
	v_cndmask_b32_e64 v80, v79, v99, s[0:1]
	v_cndmask_b32_e64 v132, v78, v98, s[0:1]
	v_mov_b32_e32 v9, v8
	v_pk_add_f32 v[74:75], v[74:75], v[76:77]
	v_mov_b32_e32 v76, 0
	v_mov_b32_e32 v77, 0
	v_mov_b32_e32 v88, 0
	v_mov_b32_e32 v91, 0
	v_mov_b32_e32 v90, 0
	v_mov_b32_e32 v89, 0
	v_mov_b32_e32 v92, 0
	v_mov_b32_e32 v95, 0
	v_mov_b32_e32 v94, 0
	v_mov_b32_e32 v93, 0
	v_cvt_pk_bf16_f32 v78, v130, v129
	v_cvt_pk_bf16_f32 v79, v87, v86
	v_cvt_pk_bf16_f32 v80, v132, v80
	v_cvt_pk_bf16_f32 v81, v131, v81
	v_add_u32_e32 v86, v121, v128
	v_mov_b32_dpp v76, v74 quad_perm:[1,0,3,2] row_mask:0xf bank_mask:0xf
	v_mov_b32_dpp v77, v75 quad_perm:[1,0,3,2] row_mask:0xf bank_mask:0xf
	v_mov_b32_dpp v88, v64 row_shr:8 row_mask:0xf bank_mask:0xf
	v_mov_b32_dpp v91, v60 row_shr:8 row_mask:0xf bank_mask:0xf
	v_mov_b32_dpp v90, v65 row_shr:8 row_mask:0xf bank_mask:0xf
	v_mov_b32_dpp v89, v61 row_shr:8 row_mask:0xf bank_mask:0xf
	v_mov_b32_dpp v92, v66 row_shr:8 row_mask:0xf bank_mask:0xf
	v_mov_b32_dpp v95, v62 row_shr:8 row_mask:0xf bank_mask:0xf
	v_mov_b32_dpp v94, v67 row_shr:8 row_mask:0xf bank_mask:0xf
	v_mov_b32_dpp v93, v63 row_shr:8 row_mask:0xf bank_mask:0xf
	ds_write2_b64 v86, v[78:79], v[80:81] offset1:16
	v_add_u32_e32 v87, v122, v115
	v_add_u32_e32 v86, v123, v115
	v_mov_b64_e32 v[80:81], v[8:9]
	v_mov_b64_e32 v[78:79], v[8:9]
	s_and_saveexec_b64 s[4:5], vcc
	s_cbranch_execz .LBB0_781
	v_pk_mul_f32 v[80:81], v[2:3], v[106:107]
	v_pk_mul_f32 v[78:79], v[0:1], v[104:105]
	ds_write_b128 v87, v[78:81] offset:16384
	v_mov_b32_e32 v78, v92
	v_mov_b32_e32 v79, v94
	v_pk_mul_f32 v[80:81], v[2:3], v[78:79]
	v_mov_b32_e32 v78, v88
	v_mov_b32_e32 v79, v90
	v_pk_mul_f32 v[78:79], v[0:1], v[78:79]
	v_and_b32_e32 v203, 0xffffff00, v86
	v_and_b32_e32 v202, 32, v86
	v_bfe_u32 v201, v86, 6, 2
	v_lshlrev_b32_e32 v202, 2, v202
	v_lshlrev_b32_e32 v201, 2, v201
	v_or3_b32 v203, v203, v202, v201
	ds_write_b32 v203, v78 offset:32768
	ds_write_b32 v203, v79 offset:32784
	ds_write_b32 v203, v80 offset:32800
	ds_write_b32 v203, v81 offset:32816
	v_mov_b32_e32 v78, v95
	v_mov_b32_e32 v79, v93
	v_pk_mul_f32 v[80:81], v[2:3], v[78:79]
	v_mov_b32_e32 v78, v91
	v_mov_b32_e32 v79, v89
	v_pk_mul_f32 v[78:79], v[0:1], v[78:79]
	ds_write_b32 v203, v78 offset:33024
	ds_write_b32 v203, v79 offset:33040
	ds_write_b32 v203, v80 offset:33056
	ds_write_b32 v203, v81 offset:33072
	ds_write_b32 v203, v64 offset:33280
	ds_write_b32 v203, v65 offset:33296
	ds_write_b32 v203, v66 offset:33312
	ds_write_b32 v203, v67 offset:33328
	ds_write_b32 v203, v60 offset:33536
	ds_write_b32 v203, v61 offset:33552
	ds_write_b32 v203, v62 offset:33568
	ds_write_b32 v203, v63 offset:33584
	v_pk_mul_f32 v[60:61], v[82:83], v[88:89] neg_lo:[1,0] neg_hi:[1,0]
	v_pk_mul_f32 v[62:63], v[100:101], v[92:93]
	v_pk_fma_f32 v[60:61], v[102:103], v[90:91], v[60:61] op_sel:[1,0,0] op_sel_hi:[0,1,1]
	v_pk_fma_f32 v[62:63], v[100:101], v[94:95], v[62:63] op_sel:[1,0,0] op_sel_hi:[0,1,1]
	v_pk_add_f32 v[60:61], v[60:61], v[62:63]
	v_pk_mul_f32 v[62:63], v[96:97], v[92:93]
	v_pk_add_f32 v[80:81], v[60:61], 0 op_sel_hi:[1,0]
	v_pk_mul_f32 v[60:61], v[98:99], v[88:89]
	v_pk_fma_f32 v[62:63], v[96:97], v[94:95], v[62:63] op_sel:[1,0,0] op_sel_hi:[0,1,1]
	v_pk_fma_f32 v[60:61], v[98:99], v[90:91], v[60:61] op_sel:[1,0,0] op_sel_hi:[0,1,1]
	v_pk_add_f32 v[60:61], v[60:61], v[62:63]
	s_nop 0
	v_pk_add_f32 v[78:79], v[60:61], 0 op_sel_hi:[1,0]
.LBB0_781:
	s_or_b64 exec, exec, s[4:5]
	v_lshlrev_b32_e32 v64, 16, v24
	v_and_b32_e32 v65, 0xffff0000, v24
	v_lshlrev_b32_e32 v66, 16, v25
	v_and_b32_e32 v67, 0xffff0000, v25
	v_lshlrev_b32_e32 v9, 16, v36
	v_and_b32_e32 v82, 0xffff0000, v36
	v_lshlrev_b32_e32 v88, 16, v37
	v_and_b32_e32 v89, 0xffff0000, v37
	s_add_i32 s2, 0, 0x14000
	v_sub_f32_e32 v83, v82, v65
	v_sub_f32_e32 v82, v9, v64
	v_sub_f32_e32 v89, v89, v67
	v_sub_f32_e32 v88, v88, v66
	v_add_u32_e32 v9, s2, v166
	s_add_i32 s2, 0, 0x1a000
	v_pk_fma_f32 v[50:51], v[88:89], v[50:51], v[66:67]
	v_pk_fma_f32 v[48:49], v[82:83], v[48:49], v[64:65]
	v_add_u32_e32 v64, s2, v166
	v_add_u32_e32 v9, v9, v115
	ds_write_b128 v9, v[48:51]
	v_add_u32_e32 v88, v64, v115
	v_mov_b32_e32 v48, v84
	v_mov_b32_e32 v49, v84
	v_pk_mul_f32 v[64:65], v[14:15], v[84:85]
	v_mov_b32_e32 v82, 0
	v_mov_b32_e32 v83, 0
	v_mov_b32_e32 v84, v8
	v_mov_b32_e32 v85, v8
	v_pk_mul_f32 v[66:67], v[68:69], v[48:49]
	v_mov_b32_dpp v82, v4 row_shr:8 row_mask:0xf bank_mask:0xf
	v_mov_b32_dpp v83, v5 row_shr:8 row_mask:0xf bank_mask:0xf
	v_mov_b32_dpp v84, v6 row_shr:8 row_mask:0xf bank_mask:0xf
	v_mov_b32_dpp v85, v7 row_shr:8 row_mask:0xf bank_mask:0xf
	v_xor_b32_e32 v91, 0x80000000, v69
	v_xor_b32_e32 v90, 0x80000000, v68
	v_xor_b32_e32 v89, 0x80000000, v14
	v_xor_b32_e32 v92, 0x80000000, v15
	v_pk_fma_f32 v[64:65], v[4:5], v[72:73], v[64:65] neg_lo:[0,0,1] neg_hi:[0,0,1]
	v_pk_fma_f32 v[66:67], v[6:7], v[70:71], v[66:67] neg_lo:[0,0,1] neg_hi:[0,0,1]
	v_pk_mul_f32 v[70:71], v[90:91], v[84:85]
	v_pk_mul_f32 v[72:73], v[14:15], v[82:83] neg_lo:[1,0] neg_hi:[1,0]
	v_lshlrev_b32_e32 v60, 16, v44
	v_and_b32_e32 v61, 0xffff0000, v44
	v_lshlrev_b32_e32 v62, 16, v45
	v_and_b32_e32 v63, 0xffff0000, v45
	v_cndmask_b32_e64 v91, v71, v91, s[0:1]
	v_cndmask_b32_e64 v90, v70, v90, s[0:1]
	v_cndmask_b32_e64 v92, v73, v92, s[0:1]
	v_cndmask_b32_e64 v89, v72, v89, s[0:1]
	v_pk_mul_f32 v[70:71], v[64:65], v[82:83]
	v_pk_mul_f32 v[72:73], v[66:67], v[84:85]
	ds_write_b128 v88, v[60:63]
	v_mov_b32_e32 v48, 0
	v_mov_b32_e32 v51, 0
	v_mov_b32_e32 v50, 0
	v_mov_b32_e32 v49, 0
	v_mov_b32_e32 v60, 0
	v_mov_b32_e32 v63, 0
	v_mov_b32_e32 v62, 0
	v_and_or_b32 v61, v120, 48, v116
	v_cndmask_b32_e64 v73, v73, v67, s[0:1]
	v_cndmask_b32_e64 v93, v72, v66, s[0:1]
	v_cndmask_b32_e64 v72, v71, v65, s[0:1]
	v_cndmask_b32_e64 v94, v70, v64, s[0:1]
	v_mov_b32_dpp v48, v56 row_shr:8 row_mask:0xf bank_mask:0xf
	v_mov_b32_dpp v51, v52 row_shr:8 row_mask:0xf bank_mask:0xf
	v_mov_b32_dpp v50, v57 row_shr:8 row_mask:0xf bank_mask:0xf
	v_mov_b32_dpp v49, v53 row_shr:8 row_mask:0xf bank_mask:0xf
	v_mov_b32_dpp v60, v58 row_shr:8 row_mask:0xf bank_mask:0xf
	v_mov_b32_dpp v63, v54 row_shr:8 row_mask:0xf bank_mask:0xf
	v_mov_b32_dpp v62, v59 row_shr:8 row_mask:0xf bank_mask:0xf
	v_mov_b32_dpp v8, v55 row_shr:8 row_mask:0xf bank_mask:0xf
	v_cvt_pk_bf16_f32 v70, v89, v92
	v_cvt_pk_bf16_f32 v71, v90, v91
	v_cvt_pk_bf16_f32 v72, v94, v72
	v_cvt_pk_bf16_f32 v73, v93, v73
	v_add_u32_e32 v61, v121, v61
	ds_write2_b64 v61, v[70:71], v[72:73] offset1:16
	s_and_saveexec_b64 s[0:1], vcc
	s_cbranch_execz .LBB0_783
	v_pk_mul_f32 v[72:73], v[6:7], v[84:85]
	v_pk_mul_f32 v[70:71], v[4:5], v[82:83]
	ds_write_b128 v87, v[70:73] offset:16400
	v_mov_b32_e32 v70, v60
	v_mov_b32_e32 v71, v62
	v_pk_mul_f32 v[72:73], v[6:7], v[70:71]
	v_mov_b32_e32 v70, v48
	v_mov_b32_e32 v71, v50
	v_pk_mul_f32 v[70:71], v[4:5], v[70:71]
	v_and_b32_e32 v203, 0xffffff00, v86
	v_and_b32_e32 v202, 32, v86
	v_bfe_u32 v201, v86, 6, 2
	v_lshlrev_b32_e32 v202, 2, v202
	v_lshlrev_b32_e32 v201, 2, v201
	v_or3_b32 v203, v203, v202, v201
	ds_write_b32 v203, v70 offset:32832
	ds_write_b32 v203, v71 offset:32848
	ds_write_b32 v203, v72 offset:32864
	ds_write_b32 v203, v73 offset:32880
	v_mov_b32_e32 v70, v63
	v_mov_b32_e32 v71, v8
	v_pk_mul_f32 v[72:73], v[6:7], v[70:71]
	v_mov_b32_e32 v70, v51
	v_mov_b32_e32 v71, v49
	v_pk_mul_f32 v[70:71], v[4:5], v[70:71]
	v_mov_b32_e32 v61, v8
	ds_write_b32 v203, v70 offset:33088
	ds_write_b32 v203, v71 offset:33104
	ds_write_b32 v203, v72 offset:33120
	ds_write_b32 v203, v73 offset:33136
	ds_write_b32 v203, v56 offset:33344
	ds_write_b32 v203, v57 offset:33360
	ds_write_b32 v203, v58 offset:33376
	ds_write_b32 v203, v59 offset:33392
	ds_write_b32 v203, v52 offset:33600
	ds_write_b32 v203, v53 offset:33616
	ds_write_b32 v203, v54 offset:33632
	ds_write_b32 v203, v55 offset:33648
	v_xor_b32_e32 v53, 0x80000000, v69
	v_xor_b32_e32 v52, 0x80000000, v68
	v_xor_b32_e32 v55, 0x80000000, v15
	v_xor_b32_e32 v54, 0x80000000, v14
	v_pk_mul_f32 v[14:15], v[14:15], v[48:49] neg_lo:[1,0] neg_hi:[1,0]
	s_nop 0
	v_pk_fma_f32 v[14:15], v[54:55], v[50:51], v[14:15] op_sel:[1,0,0] op_sel_hi:[0,1,1]
	v_pk_mul_f32 v[54:55], v[52:53], v[60:61]
	s_nop 0
	v_pk_fma_f32 v[52:53], v[52:53], v[62:63], v[54:55] op_sel:[1,0,0] op_sel_hi:[0,1,1]
	v_pk_add_f32 v[14:15], v[14:15], v[52:53]
	s_nop 0
	v_pk_add_f32 v[80:81], v[80:81], v[14:15]
	v_pk_mul_f32 v[14:15], v[64:65], v[48:49]
	v_pk_mul_f32 v[48:49], v[66:67], v[60:61]
	v_pk_fma_f32 v[14:15], v[64:65], v[50:51], v[14:15] op_sel:[1,0,0] op_sel_hi:[0,1,1]
	v_pk_fma_f32 v[48:49], v[66:67], v[62:63], v[48:49] op_sel:[1,0,0] op_sel_hi:[0,1,1]
	v_pk_add_f32 v[14:15], v[14:15], v[48:49]
	s_nop 0
	v_pk_add_f32 v[78:79], v[78:79], v[14:15]

.LBB0_796:
	s_andn2_b64 vcc, exec, s[14:15]
	s_mov_b32 s2, 64
	s_cbranch_vccnz .LBB0_805
	v_mov_b32_e32 v100, v124
	v_add_u32_e32 v108, s46, v167
	v_add_u32_e32 v100, s3, v167
	ds_read_b128 v[100:103], v100
	ds_read_b128 v[108:111], v108
	s_waitcnt vmcnt(9)
	v_lshlrev_b32_e32 v104, 16, v72
	v_and_b32_e32 v105, 0xffff0000, v72
	v_lshlrev_b32_e32 v106, 16, v73
	v_and_b32_e32 v107, 0xffff0000, v73
	s_waitcnt vmcnt(6)
	v_lshlrev_b32_e32 v49, 16, v80
	v_and_b32_e32 v122, 0xffff0000, v80
	v_lshlrev_b32_e32 v120, 16, v81
	v_and_b32_e32 v121, 0xffff0000, v81
	v_add_u32_e32 v146, s47, v167
	v_sub_f32_e32 v121, v121, v107
	v_sub_f32_e32 v120, v120, v106
	v_sub_f32_e32 v123, v122, v105
	v_sub_f32_e32 v122, v49, v104
	s_waitcnt lgkmcnt(1)
	v_pk_fma_f32 v[138:139], v[122:123], v[100:101], v[104:105]
	v_pk_fma_f32 v[140:141], v[120:121], v[102:103], v[106:107]
	v_add_u32_e32 v49, s48, v167
	ds_read_b128 v[104:107], v146
	ds_read_b128 v[100:103], v49
	v_lshlrev_b32_e32 v116, 16, v68
	v_and_b32_e32 v117, 0xffff0000, v68
	s_waitcnt vmcnt(5)
	v_lshlrev_b32_e32 v142, 16, v88
	v_and_b32_e32 v143, 0xffff0000, v88
	v_lshlrev_b32_e32 v118, 16, v69
	v_and_b32_e32 v119, 0xffff0000, v69
	v_lshlrev_b32_e32 v144, 16, v89
	v_and_b32_e32 v145, 0xffff0000, v89
	v_sub_f32_e32 v123, v143, v117
	v_sub_f32_e32 v122, v142, v116
	v_sub_f32_e32 v121, v145, v119
	v_sub_f32_e32 v120, v144, v118
	s_waitcnt lgkmcnt(2)
	v_pk_fma_f32 v[144:145], v[122:123], v[108:109], v[116:117]
	v_add_u32_e32 v49, s3, v168
	v_pk_fma_f32 v[146:147], v[120:121], v[110:111], v[118:119]
	s_waitcnt lgkmcnt(0)
	v_pk_mul_f32 v[142:143], v[144:145], v[100:101]
	v_add_u32_e32 v100, s46, v168
	ds_read_b128 v[108:111], v49
	ds_read_b128 v[116:119], v100
	v_add_u32_e32 v49, s47, v168
	v_add_u32_e32 v120, s48, v168
	v_pk_mul_f32 v[148:149], v[146:147], v[102:103]
	ds_read_b128 v[100:103], v49
	ds_read_b128 v[120:123], v120
	v_lshlrev_b32_e32 v130, 16, v70
	v_and_b32_e32 v131, 0xffff0000, v70
	v_lshlrev_b32_e32 v152, 16, v90
	v_and_b32_e32 v153, 0xffff0000, v90
	v_lshlrev_b32_e32 v134, 16, v71
	v_and_b32_e32 v135, 0xffff0000, v71
	v_lshlrev_b32_e32 v150, 16, v91
	v_and_b32_e32 v151, 0xffff0000, v91
	v_sub_f32_e32 v153, v153, v131
	v_sub_f32_e32 v152, v152, v130
	v_sub_f32_e32 v151, v151, v135
	v_sub_f32_e32 v150, v150, v134
	s_waitcnt lgkmcnt(2)
	v_pk_fma_f32 v[152:153], v[152:153], v[116:117], v[130:131]
	v_pk_fma_f32 v[150:151], v[150:151], v[118:119], v[134:135]
	s_waitcnt lgkmcnt(0)
	v_pk_mul_f32 v[156:157], v[152:153], v[120:121]
	v_pk_mul_f32 v[154:155], v[150:151], v[122:123]
	v_mov_b32_e32 v118, v143
	v_mov_b32_e32 v119, v157
	v_mov_b32_e32 v116, v142
	v_mov_b32_e32 v117, v156
	v_pk_mul_f32 v[118:119], v[118:119], v[118:119]
	v_mov_b32_e32 v120, v149
	v_mov_b32_e32 v121, v155
	v_pk_fma_f32 v[116:117], v[116:117], v[116:117], v[118:119]
	v_mov_b32_e32 v118, v148
	v_mov_b32_e32 v119, v154
	v_pk_mul_f32 v[120:121], v[120:121], v[120:121]
	s_mov_b32 s2, 0xf800000
	v_pk_fma_f32 v[118:119], v[118:119], v[118:119], v[120:121]
	v_lshlrev_b32_e32 v128, 16, v74
	v_pk_add_f32 v[116:117], v[116:117], v[118:119]
	v_and_b32_e32 v129, 0xffff0000, v74
	v_add_f32_e32 v49, v116, v117
	v_lshlrev_b32_e32 v158, 16, v82
	v_and_b32_e32 v159, 0xffff0000, v82
	v_add_f32_dpp v49, v49, v49 row_half_mirror row_mask:0xf bank_mask:0xf bound_ctrl:1
	v_sub_f32_e32 v119, v159, v129
	v_lshlrev_b32_e32 v132, 16, v75
	v_add_f32_dpp v49, v49, v49 quad_perm:[3,2,1,0] row_mask:0xf bank_mask:0xf bound_ctrl:1
	v_and_b32_e32 v133, 0xffff0000, v75
	v_lshlrev_b32_e32 v160, 16, v83
	v_add_f32_dpp v49, v49, v49 quad_perm:[1,0,3,2] row_mask:0xf bank_mask:0xf bound_ctrl:1
	v_mul_f32_e32 v116, 0x4f800000, v49
	v_cmp_gt_f32_e32 vcc, s2, v49
	v_and_b32_e32 v161, 0xffff0000, v83
	v_sub_f32_e32 v117, v161, v133
	v_cndmask_b32_e32 v49, v49, v116, vcc
	v_sqrt_f32_e32 v118, v49
	v_sub_f32_e32 v116, v160, v132
	s_waitcnt vmcnt(3)
	v_lshlrev_b32_e32 v50, 16, v92
	v_and_b32_e32 v51, 0xffff0000, v92
	v_add_u32_e32 v120, -1, v118
	v_fma_f32 v121, -v120, v118, v49
	v_cmp_ge_f32_e64 s[14:15], 0, v121
	v_add_u32_e32 v121, 1, v118
	v_lshlrev_b32_e32 v136, 16, v93
	v_cndmask_b32_e64 v120, v118, v120, s[14:15]
	v_fma_f32 v118, -v121, v118, v49
	v_cmp_lt_f32_e64 s[14:15], 0, v118
	v_and_b32_e32 v137, 0xffff0000, v93
	v_lshlrev_b32_e32 v112, 16, v94
	v_cndmask_b32_e64 v118, v120, v121, s[14:15]
	v_mul_f32_e32 v120, 0x37800000, v118
	v_cndmask_b32_e32 v118, v118, v120, vcc
	v_cmp_class_f32_e32 vcc, v49, v192
	v_and_b32_e32 v113, 0xffff0000, v94
	v_lshlrev_b32_e32 v114, 16, v95
	v_cndmask_b32_e32 v49, v118, v49, vcc
	v_max_f32_e32 v49, 0x2b8cbccc, v49
	v_div_scale_f32 v120, s[14:15], v49, v49, 1.0
	v_rcp_f32_e32 v121, v120
	v_sub_f32_e32 v118, v158, v128
	v_pk_fma_f32 v[130:131], v[118:119], v[108:109], v[128:129]
	v_pk_fma_f32 v[128:129], v[116:117], v[110:111], v[132:133]
	v_fma_f32 v108, -v120, v121, 1.0
	v_fmac_f32_e32 v121, v108, v121
	v_div_scale_f32 v108, vcc, 1.0, v49, 1.0
	v_mul_f32_e32 v109, v108, v121
	v_fma_f32 v110, -v120, v109, v108
	v_fmac_f32_e32 v109, v110, v121
	v_fma_f32 v108, -v120, v109, v108
	v_div_fmas_f32 v108, v108, v121, v109
	v_div_fixup_f32 v158, v108, v49, 1.0
	v_add_u32_e32 v49, s49, v167
	ds_read_b128 v[108:111], v49
	v_pk_add_f32 v[116:117], v[50:51], -1.0 op_sel_hi:[1,0]
	v_pk_add_f32 v[118:119], v[136:137], -1.0 op_sel_hi:[1,0]
	v_add_u32_e32 v49, s50, v167
	ds_read_b128 v[132:135], v49
	s_waitcnt lgkmcnt(1)
	v_pk_fma_f32 v[110:111], v[118:119], v[110:111], 1.0 op_sel_hi:[1,1,0]
	v_pk_fma_f32 v[108:109], v[116:117], v[108:109], 1.0 op_sel_hi:[1,1,0]
	v_add_u32_e32 v49, s49, v168
	v_pk_mul_f32 v[118:119], v[146:147], v[110:111]
	v_pk_mul_f32 v[116:117], v[144:145], v[108:109]
	ds_read_b128 v[108:111], v49
	v_pk_mul_f32 v[142:143], v[142:143], v[158:159] op_sel_hi:[1,0]
	v_and_b32_e32 v115, 0xffff0000, v95
	v_pk_mul_f32 v[194:195], v[148:149], v[158:159] op_sel_hi:[1,0]
	v_pk_mul_f32 v[120:121], v[142:143], v[50:51]
	v_pk_mul_f32 v[50:51], v[156:157], v[158:159] op_sel_hi:[1,0]
	v_pk_add_f32 v[144:145], v[112:113], -1.0 op_sel_hi:[1,0]
	v_pk_mul_f32 v[122:123], v[194:195], v[136:137]
	v_pk_mul_f32 v[136:137], v[154:155], v[158:159] op_sel_hi:[1,0]
	v_pk_add_f32 v[154:155], v[114:115], -1.0 op_sel_hi:[1,0]
	s_waitcnt lgkmcnt(0)
	v_pk_fma_f32 v[108:109], v[144:145], v[108:109], 1.0 op_sel_hi:[1,1,0]
	v_pk_mul_f32 v[112:113], v[50:51], v[112:113]
	v_pk_fma_f32 v[110:111], v[154:155], v[110:111], 1.0 op_sel_hi:[1,1,0]
	v_pk_mul_f32 v[108:109], v[152:153], v[108:109]
	v_pk_mul_f32 v[114:115], v[136:137], v[114:115]
	v_mov_b32_e32 v152, v131
	v_mov_b32_e32 v153, v139
	v_mov_b32_e32 v154, v113
	v_mov_b32_e32 v155, v121
	v_pk_mul_f32 v[110:111], v[150:151], v[110:111]
	v_mov_b32_e32 v144, v130
	v_mov_b32_e32 v145, v138
	v_mov_b32_e32 v150, v112
	v_mov_b32_e32 v151, v120
	v_pk_mul_f32 v[152:153], v[152:153], v[154:155]
	v_mov_b32_e32 v154, v129
	v_mov_b32_e32 v155, v141
	v_mov_b32_e32 v156, v115
	v_mov_b32_e32 v157, v123
	v_pk_mul_f32 v[162:163], v[138:139], v[116:117]
	v_add_u32_e32 v49, s50, v168
	v_pk_fma_f32 v[144:145], v[144:145], v[150:151], v[152:153]
	v_mov_b32_e32 v150, v128
	v_mov_b32_e32 v151, v140
	v_mov_b32_e32 v152, v114
	v_mov_b32_e32 v153, v122
	v_pk_mul_f32 v[154:155], v[154:155], v[156:157]
	ds_read_b128 v[146:149], v49
	v_pk_fma_f32 v[150:151], v[150:151], v[152:153], v[154:155]
	v_mov_b32_e32 v155, v132
	v_mov_b32_e32 v157, v162
	v_mov_b32_e32 v132, v139
	v_mov_b32_e32 v162, v117
	v_pk_mul_f32 v[160:161], v[140:141], v[118:119]
	v_mov_b32_e32 v154, v138
	v_mov_b32_e32 v156, v116
	v_pk_mul_f32 v[132:133], v[132:133], v[162:163]
	v_pk_mul_f32 v[152:153], v[130:131], v[108:109]
	v_pk_fma_f32 v[132:133], v[154:155], v[156:157], v[132:133]
	v_pk_mov_b32 v[154:155], v[140:141], v[134:135] op_sel:[1,0]
	v_pk_mov_b32 v[156:157], v[118:119], v[160:161] op_sel:[1,0]
	v_mov_b32_e32 v134, v140
	v_mov_b32_e32 v160, v118
	v_pk_mul_f32 v[134:135], v[134:135], v[160:161]
	v_pk_add_f32 v[144:145], v[144:145], v[150:151]
	v_pk_fma_f32 v[134:135], v[154:155], v[156:157], v[134:135]
	v_mov_b32_e32 v155, v152
	v_pk_add_f32 v[132:133], v[132:133], v[134:135]
	s_waitcnt lgkmcnt(0)
	v_mov_b32_e32 v135, v146
	v_mov_b32_e32 v146, v131
	v_mov_b32_e32 v152, v109
	v_add_f32_e32 v49, 0, v145
	v_pk_mul_f32 v[150:151], v[128:129], v[110:111]
	v_mov_b32_e32 v134, v130
	v_mov_b32_e32 v154, v108
	v_pk_mul_f32 v[146:147], v[146:147], v[152:153]
	v_add_f32_e32 v49, v144, v49
	v_pk_fma_f32 v[134:135], v[134:135], v[154:155], v[146:147]
	v_pk_mov_b32 v[146:147], v[128:129], v[148:149] op_sel:[1,0]
	v_pk_mov_b32 v[152:153], v[110:111], v[150:151] op_sel:[1,0]
	v_mov_b32_e32 v148, v128
	v_mov_b32_e32 v150, v110
	s_and_b32 s44, s52, 1
	v_add_f32_dpp v49, v49, v49 row_half_mirror row_mask:0xf bank_mask:0xf bound_ctrl:1
	v_pk_mul_f32 v[148:149], v[148:149], v[150:151]
	s_lshl_b32 s2, s44, 13
	v_add_f32_dpp v49, v49, v49 quad_perm:[3,2,1,0] row_mask:0xf bank_mask:0xf bound_ctrl:1
	v_pk_fma_f32 v[146:147], v[146:147], v[152:153], v[148:149]
	v_pk_add_f32 v[132:133], v[132:133], 0 op_sel_hi:[1,0]
	v_add_f32_dpp v144, v49, v49 quad_perm:[1,0,3,2] row_mask:0xf bank_mask:0xf bound_ctrl:1
	v_pk_add_f32 v[134:135], v[134:135], v[146:147]
	v_add_u32_e32 v145, s2, v172
	v_mov_b32_e32 v162, 0
	v_mov_b32_e32 v163, 0
	v_mov_b32_e32 v164, v48
	v_mov_b32_e32 v165, v48
	v_pk_add_f32 v[132:133], v[132:133], v[134:135]
	v_mov_b32_e32 v134, v48
	v_mov_b32_e32 v135, v48
	v_pk_mul_f32 v[156:157], v[142:143], v[144:145] op_sel_hi:[1,0]
	v_pk_mul_f32 v[154:155], v[194:195], v[144:145] op_sel_hi:[1,0]
	s_waitcnt vmcnt(0)
	v_mov_b32_dpp v162, v8 row_shr:8 row_mask:0xf bank_mask:0xf
	v_mov_b32_dpp v163, v9 row_shr:8 row_mask:0xf bank_mask:0xf
	v_mov_b32_dpp v164, v10 row_shr:8 row_mask:0xf bank_mask:0xf
	v_mov_b32_dpp v165, v11 row_shr:8 row_mask:0xf bank_mask:0xf
	v_mov_b32_dpp v134, v132 row_half_mirror row_mask:0xf bank_mask:0xf
	v_mov_b32_dpp v135, v133 row_half_mirror row_mask:0xf bank_mask:0xf
	v_xor_b32_e32 v160, 0x80000000, v142
	v_xor_b32_e32 v161, 0x80000000, v143
	v_xor_b32_e32 v158, 0x80000000, v194
	v_xor_b32_e32 v159, 0x80000000, v195
	v_pk_fma_f32 v[154:155], v[10:11], v[140:141], v[154:155] neg_lo:[0,0,1] neg_hi:[0,0,1]
	v_pk_fma_f32 v[156:157], v[8:9], v[138:139], v[156:157] neg_lo:[0,0,1] neg_hi:[0,0,1]
	v_pk_mul_f32 v[138:139], v[142:143], v[162:163] neg_lo:[1,0] neg_hi:[1,0]
	v_pk_mul_f32 v[140:141], v[194:195], v[164:165] neg_lo:[1,0] neg_hi:[1,0]
	v_pk_add_f32 v[132:133], v[132:133], v[134:135]
	v_mov_b32_e32 v134, v48
	v_mov_b32_e32 v135, v48
	v_cndmask_b32_e64 v194, v141, v159, s[0:1]
	v_cndmask_b32_e64 v195, v140, v158, s[0:1]
	v_cndmask_b32_e64 v197, v139, v161, s[0:1]
	v_cndmask_b32_e64 v198, v138, v160, s[0:1]
	v_pk_mul_f32 v[138:139], v[156:157], v[162:163]
	v_pk_mul_f32 v[140:141], v[154:155], v[164:165]
	v_mov_b32_dpp v134, v132 quad_perm:[3,2,1,0] row_mask:0xf bank_mask:0xf
	v_mov_b32_dpp v135, v133 quad_perm:[3,2,1,0] row_mask:0xf bank_mask:0xf
	v_add_u32_e32 v193, s2, v171
	v_cndmask_b32_e64 v141, v141, v155, s[0:1]
	v_cndmask_b32_e64 v199, v140, v154, s[0:1]
	v_cndmask_b32_e64 v140, v139, v157, s[0:1]
	v_cndmask_b32_e64 v200, v138, v156, s[0:1]
	v_mov_b32_e32 v49, v48
	v_pk_add_f32 v[132:133], v[132:133], v[134:135]
	v_mov_b32_e32 v134, 0
	v_mov_b32_e32 v135, 0
	v_lshl_add_u32 v196, s44, 14, v173
	v_mov_b32_e32 v146, 0
	v_mov_b32_e32 v149, 0
	v_mov_b32_e32 v148, 0
	v_mov_b32_e32 v147, 0
	v_mov_b32_e32 v150, 0
	v_mov_b32_e32 v153, 0
	v_mov_b32_e32 v152, 0
	v_mov_b32_e32 v151, 0
	v_cvt_pk_bf16_f32 v138, v198, v197
	v_cvt_pk_bf16_f32 v139, v195, v194
	v_cvt_pk_bf16_f32 v140, v200, v140
	v_cvt_pk_bf16_f32 v141, v199, v141
	v_add_u32_e32 v194, v193, v183
	v_mov_b32_dpp v134, v132 quad_perm:[1,0,3,2] row_mask:0xf bank_mask:0xf
	v_mov_b32_dpp v135, v133 quad_perm:[1,0,3,2] row_mask:0xf bank_mask:0xf
	v_mov_b32_dpp v146, v120 row_shr:8 row_mask:0xf bank_mask:0xf
	v_mov_b32_dpp v149, v116 row_shr:8 row_mask:0xf bank_mask:0xf
	v_mov_b32_dpp v148, v121 row_shr:8 row_mask:0xf bank_mask:0xf
	v_mov_b32_dpp v147, v117 row_shr:8 row_mask:0xf bank_mask:0xf
	v_mov_b32_dpp v150, v122 row_shr:8 row_mask:0xf bank_mask:0xf
	v_mov_b32_dpp v153, v118 row_shr:8 row_mask:0xf bank_mask:0xf
	v_mov_b32_dpp v152, v123 row_shr:8 row_mask:0xf bank_mask:0xf
	v_mov_b32_dpp v151, v119 row_shr:8 row_mask:0xf bank_mask:0xf
	ds_write2_b64 v194, v[138:139], v[140:141] offset1:16
	v_add_u32_e32 v195, v145, v167
	v_add_u32_e32 v194, v196, v167
	v_mov_b64_e32 v[140:141], v[48:49]
	v_mov_b64_e32 v[138:139], v[48:49]
	s_and_saveexec_b64 s[14:15], s[4:5]
	s_cbranch_execz .LBB0_799
	v_pk_mul_f32 v[140:141], v[10:11], v[164:165]
	v_pk_mul_f32 v[138:139], v[8:9], v[162:163]
	ds_write_b128 v195, v[138:141] offset:16384
	v_mov_b32_e32 v138, v150
	v_mov_b32_e32 v139, v152
	v_pk_mul_f32 v[140:141], v[10:11], v[138:139]
	v_mov_b32_e32 v138, v146
	v_mov_b32_e32 v139, v148
	v_pk_mul_f32 v[138:139], v[8:9], v[138:139]
	v_and_b32_e32 v203, 0xffffff00, v194
	v_and_b32_e32 v202, 32, v194
	v_bfe_u32 v201, v194, 6, 2
	v_lshlrev_b32_e32 v202, 2, v202
	v_lshlrev_b32_e32 v201, 2, v201
	v_or3_b32 v203, v203, v202, v201
	ds_write_b32 v203, v138 offset:32768
	ds_write_b32 v203, v139 offset:32784
	ds_write_b32 v203, v140 offset:32800
	ds_write_b32 v203, v141 offset:32816
	v_mov_b32_e32 v138, v153
	v_mov_b32_e32 v139, v151
	v_pk_mul_f32 v[140:141], v[10:11], v[138:139]
	v_mov_b32_e32 v138, v149
	v_mov_b32_e32 v139, v147
	v_pk_mul_f32 v[138:139], v[8:9], v[138:139]
	ds_write_b32 v203, v138 offset:33024
	ds_write_b32 v203, v139 offset:33040
	ds_write_b32 v203, v140 offset:33056
	ds_write_b32 v203, v141 offset:33072
	ds_write_b32 v203, v120 offset:33280
	ds_write_b32 v203, v121 offset:33296
	ds_write_b32 v203, v122 offset:33312
	ds_write_b32 v203, v123 offset:33328
	ds_write_b32 v203, v116 offset:33536
	ds_write_b32 v203, v117 offset:33552
	ds_write_b32 v203, v118 offset:33568
	ds_write_b32 v203, v119 offset:33584
	v_pk_mul_f32 v[116:117], v[142:143], v[146:147] neg_lo:[1,0] neg_hi:[1,0]
	v_pk_mul_f32 v[118:119], v[158:159], v[150:151]
	v_pk_fma_f32 v[116:117], v[160:161], v[148:149], v[116:117] op_sel:[1,0,0] op_sel_hi:[0,1,1]
	v_pk_fma_f32 v[118:119], v[158:159], v[152:153], v[118:119] op_sel:[1,0,0] op_sel_hi:[0,1,1]
	v_pk_add_f32 v[116:117], v[116:117], v[118:119]
	v_pk_mul_f32 v[118:119], v[154:155], v[150:151]
	v_pk_add_f32 v[140:141], v[116:117], 0 op_sel_hi:[1,0]
	v_pk_mul_f32 v[116:117], v[156:157], v[146:147]
	v_pk_fma_f32 v[118:119], v[154:155], v[152:153], v[118:119] op_sel:[1,0,0] op_sel_hi:[0,1,1]
	v_pk_fma_f32 v[116:117], v[156:157], v[148:149], v[116:117] op_sel:[1,0,0] op_sel_hi:[0,1,1]
	v_pk_add_f32 v[116:117], v[116:117], v[118:119]
	s_nop 0
	v_pk_add_f32 v[138:139], v[116:117], 0 op_sel_hi:[1,0]
.LBB0_799:
	s_or_b64 exec, exec, s[14:15]
	s_mul_hi_u32 s2, s52, 0xaaaaaaab
	s_lshr_b32 s2, s2, 1
	s_mul_i32 s2, s2, 3
	v_lshlrev_b32_e32 v120, 16, v76
	v_and_b32_e32 v121, 0xffff0000, v76
	v_lshlrev_b32_e32 v122, 16, v77
	v_and_b32_e32 v123, 0xffff0000, v77
	v_lshlrev_b32_e32 v49, 16, v84
	v_and_b32_e32 v142, 0xffff0000, v84
	v_lshlrev_b32_e32 v146, 16, v85
	v_and_b32_e32 v147, 0xffff0000, v85
	s_sub_i32 s2, s52, s2
	v_sub_f32_e32 v143, v142, v121
	v_sub_f32_e32 v142, v49, v120
	v_sub_f32_e32 v147, v147, v123
	v_sub_f32_e32 v146, v146, v122
	s_lshl_b32 s14, s2, 13
	v_mov_b32_e32 v145, v144
	v_pk_fma_f32 v[106:107], v[146:147], v[106:107], v[122:123]
	v_pk_fma_f32 v[104:105], v[142:143], v[104:105], v[120:121]
	v_add_u32_e32 v49, s14, v177
	ds_write_b128 v49, v[104:107]
	v_mov_b32_e32 v104, v144
	v_mov_b32_e32 v105, v144
	v_pk_mul_f32 v[120:121], v[50:51], v[144:145]
	v_mov_b32_e32 v144, 0
	v_mov_b32_e32 v145, 0
	v_mov_b32_e32 v146, 0
	v_mov_b32_e32 v147, 0
	v_pk_mul_f32 v[122:123], v[136:137], v[104:105]
	v_mov_b32_dpp v144, v12 row_shr:8 row_mask:0xf bank_mask:0xf
	v_mov_b32_dpp v145, v13 row_shr:8 row_mask:0xf bank_mask:0xf
	v_mov_b32_dpp v146, v14 row_shr:8 row_mask:0xf bank_mask:0xf
	v_mov_b32_dpp v147, v15 row_shr:8 row_mask:0xf bank_mask:0xf
	v_xor_b32_e32 v137, 0x80000000, v137
	v_xor_b32_e32 v136, 0x80000000, v136
	v_xor_b32_e32 v142, 0x80000000, v50
	v_xor_b32_e32 v143, 0x80000000, v51
	v_pk_fma_f32 v[120:121], v[12:13], v[130:131], v[120:121] neg_lo:[0,0,1] neg_hi:[0,0,1]
	v_pk_fma_f32 v[122:123], v[14:15], v[128:129], v[122:123] neg_lo:[0,0,1] neg_hi:[0,0,1]
	v_pk_mul_f32 v[128:129], v[136:137], v[146:147]
	v_pk_mul_f32 v[130:131], v[50:51], v[144:145] neg_lo:[1,0] neg_hi:[1,0]
	v_lshlrev_b32_e32 v116, 16, v96
	v_and_b32_e32 v117, 0xffff0000, v96
	v_lshlrev_b32_e32 v118, 16, v97
	v_and_b32_e32 v119, 0xffff0000, v97
	v_add_u32_e32 v148, s14, v169
	v_cndmask_b32_e64 v149, v129, v137, s[0:1]
	v_cndmask_b32_e64 v150, v128, v136, s[0:1]
	v_cndmask_b32_e64 v151, v131, v143, s[0:1]
	v_cndmask_b32_e64 v152, v130, v142, s[0:1]
	v_pk_mul_f32 v[128:129], v[120:121], v[144:145]
	v_pk_mul_f32 v[130:131], v[122:123], v[146:147]
	ds_write_b128 v148, v[116:119]
	v_mov_b32_e32 v104, 0
	v_mov_b32_e32 v107, 0
	v_mov_b32_e32 v106, 0
	v_mov_b32_e32 v105, 0
	v_mov_b32_e32 v116, 0
	v_mov_b32_e32 v119, 0
	v_mov_b32_e32 v118, 0
	v_mov_b32_e32 v117, 0
	v_cndmask_b32_e64 v131, v131, v123, s[0:1]
	v_cndmask_b32_e64 v153, v130, v122, s[0:1]
	v_cndmask_b32_e64 v130, v129, v121, s[0:1]
	v_cndmask_b32_e64 v154, v128, v120, s[0:1]
	v_mov_b32_dpp v104, v112 row_shr:8 row_mask:0xf bank_mask:0xf
	v_mov_b32_dpp v107, v108 row_shr:8 row_mask:0xf bank_mask:0xf
	v_mov_b32_dpp v106, v113 row_shr:8 row_mask:0xf bank_mask:0xf
	v_mov_b32_dpp v105, v109 row_shr:8 row_mask:0xf bank_mask:0xf
	v_mov_b32_dpp v116, v114 row_shr:8 row_mask:0xf bank_mask:0xf
	v_mov_b32_dpp v119, v110 row_shr:8 row_mask:0xf bank_mask:0xf
	v_mov_b32_dpp v118, v115 row_shr:8 row_mask:0xf bank_mask:0xf
	v_mov_b32_dpp v117, v111 row_shr:8 row_mask:0xf bank_mask:0xf
	v_cvt_pk_bf16_f32 v128, v152, v151
	v_cvt_pk_bf16_f32 v129, v150, v149
	v_cvt_pk_bf16_f32 v130, v154, v130
	v_cvt_pk_bf16_f32 v131, v153, v131
	v_add_u32_e32 v149, v193, v184
	ds_write2_b64 v149, v[128:129], v[130:131] offset1:16
	s_and_saveexec_b64 s[14:15], s[4:5]
	s_cbranch_execz .LBB0_801
	v_pk_mul_f32 v[130:131], v[14:15], v[146:147]
	v_pk_mul_f32 v[128:129], v[12:13], v[144:145]
	ds_write_b128 v195, v[128:131] offset:16400
	v_mov_b32_e32 v128, v116
	v_mov_b32_e32 v129, v118
	v_pk_mul_f32 v[130:131], v[14:15], v[128:129]
	v_mov_b32_e32 v128, v104
	v_mov_b32_e32 v129, v106
	v_pk_mul_f32 v[128:129], v[12:13], v[128:129]
	v_and_b32_e32 v203, 0xffffff00, v194
	v_and_b32_e32 v202, 32, v194
	v_bfe_u32 v201, v194, 6, 2
	v_lshlrev_b32_e32 v202, 2, v202
	v_lshlrev_b32_e32 v201, 2, v201
	v_or3_b32 v203, v203, v202, v201
	ds_write_b32 v203, v128 offset:32832
	ds_write_b32 v203, v129 offset:32848
	ds_write_b32 v203, v130 offset:32864
	ds_write_b32 v203, v131 offset:32880
	v_mov_b32_e32 v128, v119
	v_mov_b32_e32 v129, v117
	v_pk_mul_f32 v[130:131], v[14:15], v[128:129]
	v_mov_b32_e32 v128, v107
	v_mov_b32_e32 v129, v105
	v_pk_mul_f32 v[128:129], v[12:13], v[128:129]
	ds_write_b32 v203, v128 offset:33088
	ds_write_b32 v203, v129 offset:33104
	ds_write_b32 v203, v130 offset:33120
	ds_write_b32 v203, v131 offset:33136
	ds_write_b32 v203, v112 offset:33344
	ds_write_b32 v203, v113 offset:33360
	ds_write_b32 v203, v114 offset:33376
	ds_write_b32 v203, v115 offset:33392
	ds_write_b32 v203, v108 offset:33600
	ds_write_b32 v203, v109 offset:33616
	ds_write_b32 v203, v110 offset:33632
	ds_write_b32 v203, v111 offset:33648
	v_pk_mul_f32 v[50:51], v[50:51], v[104:105] neg_lo:[1,0] neg_hi:[1,0]
	v_pk_mul_f32 v[108:109], v[136:137], v[116:117]
	v_pk_fma_f32 v[50:51], v[142:143], v[106:107], v[50:51] op_sel:[1,0,0] op_sel_hi:[0,1,1]
	v_pk_fma_f32 v[108:109], v[136:137], v[118:119], v[108:109] op_sel:[1,0,0] op_sel_hi:[0,1,1]
	v_pk_add_f32 v[50:51], v[50:51], v[108:109]
	s_nop 0
	v_pk_add_f32 v[140:141], v[140:141], v[50:51]
	v_pk_mul_f32 v[50:51], v[120:121], v[104:105]
	v_pk_mul_f32 v[104:105], v[122:123], v[116:117]
	v_pk_fma_f32 v[50:51], v[120:121], v[106:107], v[50:51] op_sel:[1,0,0] op_sel_hi:[0,1,1]
	v_pk_fma_f32 v[104:105], v[122:123], v[118:119], v[104:105] op_sel:[1,0,0] op_sel_hi:[0,1,1]
	v_pk_add_f32 v[50:51], v[50:51], v[104:105]
	s_nop 0
	v_pk_add_f32 v[138:139], v[138:139], v[50:51]

; #define LAS __attribute__((address_space(3)))
; __device__ __forceinline__ void scan_head(const Params& p, LAS unsigned char* lds, int bh, const int wave) {
;     ...
;             const int bp = chunk & 1, vb = chunk % 3;
;             const LAS unsigned char* awp = lds + L_AW + bp * 8192 + sel * 128 + rg * 16;
;             const LAS unsigned char* wwp = lds + L_W + bp * 8192 + rg * 16;
;             const LAS unsigned char* abp = lds + L_BK + bp * 16384 + rg * 256 + ri * 4;
;             const LAS unsigned char* vp = lds + L_V + vb * 8192 + (16 * wave + ri) * 4;
;             const LAS unsigned char* csp = lds + L_CS + bp * 256;
;             LAS unsigned char* yp = (rg == 0) ? (lds + L_Y + bp * 8192 + (16 * wave + ri) * 4) : ((rg == 2) ? (lds + L_Y + bp * 8192 + 256 + (16 * wave + ri) * 4) : (lds + L_DUMMY + tid * 4));
;             const int y_st = (rg & 1) ? 0 : 512;
;     ...
;             bf16x8 Pa0, Pa1, Qa0, Qa1; f32x4 Pw0, Pw1, Pw2, Pw3, Qw0, Qw1, Qw2, Qw3, Pcs, Qcs; float Pb0, Pb1, Pb2, Pb3, Pvt, Pvu, Qb0, Qb1, Qb2, Qb3, Qvt, Qvu;
;             SCAN_LD(P, 0);
; #pragma unroll 1
;             for (int pi = 0; pi < 16; pi += 2) {
;                 SCAN_LD(Q, pi + 1);
;                 SCAN_STEP(P, pi);
;                 if (pi + 2 < 16) SCAN_LD(P, pi + 2);
;                 SCAN_STEP(Q, pi + 1);
.LBB0_806:
	s_and_b64 vcc, exec, s[14:15]
	s_cbranch_vccz .LBB0_789
	s_setprio 3
	s_and_b32 s2, s51, 1
	s_lshl_b32 s15, s2, 13
	s_mul_i32 s14, s51, 0xab
	s_lshl_b32 s52, s2, 14
	s_bfe_u32 s14, s14, 0x70009
	s_lshl_b32 s44, s2, 8
	s_mul_i32 s14, s14, 3
	s_waitcnt vmcnt(0)
	s_sub_i32 s14, s51, s14
	s_and_b32 s14, s14, 0xff
	s_lshl_b32 s14, s14, 13
	s_add_i32 s44, s44, 0x20300
	v_add_u32_e32 v98, s15, v176
	v_add_u32_e32 v99, s15, v175
	v_and_b32_e32 v204, 0x300, v178
	v_and_b32_e32 v0, 60, v178
	v_lshl_add_u32 v0, v0, 2, v204
	v_add_u32_e32 v0, s52, v0
	v_add_u32_e32 v1, s14, v179
	v_add_u32_e32 v0, 0x8000, v0
	v_add_u32_e32 v4, 0x100, v1
	v_mov_b32_e32 v2, s44
	v_cndmask_b32_e64 v4, v4, v1, s[8:9]
	v_cndmask_b32_e64 v4, v4, v1, s[12:13]
	v_cndmask_b32_e64 v1, v4, v1, s[10:11]
	v_add_u32_e32 v4, s15, v181
	v_add_u32_e32 v6, 0xd00, v180
	v_add_u32_e32 v5, 0x100, v4
	v_cndmask_b32_e64 v5, v6, v5, s[10:11]
	v_cndmask_b32_e64 v3, v5, v4, s[8:9]
	ds_read_b128 v[68:71], v98 offset:0
	ds_read_b128 v[72:75], v98 offset:64
	ds_read_b128 v[76:79], v99 offset:16384
	ds_read_b128 v[80:83], v99 offset:16448
	ds_read_b128 v[84:87], v99 offset:16512
	ds_read_b128 v[88:91], v99 offset:16576
	ds_read_b128 v[92:95], v0 offset:0
	ds_read_b32 v96, v1 offset:0
	ds_read_b128 v[100:103], v2 offset:0
	v_cvt_pk_bf16_f32 v8, v64, v65
	v_cvt_pk_bf16_f32 v9, v66, v67
	v_cvt_pk_bf16_f32 v10, v60, v61
	v_cvt_pk_bf16_f32 v11, v62, v63
	v_cvt_pk_bf16_f32 v12, v52, v53
	v_cvt_pk_bf16_f32 v13, v54, v55
	s_waitcnt lgkmcnt(3)
	v_mfma_f32_16x16x32_bf16 v[140:143], v[68:71], v[8:11], 0
	v_cvt_pk_bf16_f32 v14, v56, v57
	v_cvt_pk_bf16_f32 v15, v58, v59
	v_pk_mul_f32 v[64:65], v[64:65], v[76:77]
	v_pk_mul_f32 v[66:67], v[66:67], v[78:79]
	v_mfma_f32_16x16x32_bf16 v[140:143], v[72:75], v[12:15], v[140:143]
	v_pk_mul_f32 v[60:61], v[60:61], v[80:81]
	v_pk_mul_f32 v[62:63], v[62:63], v[82:83]
	v_pk_mul_f32 v[52:53], v[52:53], v[84:85]
	v_pk_mul_f32 v[54:55], v[54:55], v[86:87]
	v_pk_mul_f32 v[56:57], v[56:57], v[88:89]
	v_pk_mul_f32 v[58:59], v[58:59], v[90:91]
	ds_read_b128 v[104:107], v98 offset:512
	ds_read_b128 v[108:111], v98 offset:576
	ds_read_b128 v[112:115], v99 offset:16640
	ds_read_b128 v[116:119], v99 offset:16704
	ds_read_b128 v[120:123], v99 offset:16768
	ds_read_b128 v[128:131], v99 offset:16832
	s_waitcnt lgkmcnt(6)
	v_fma_f32 v144, v100, v140, v142
	v_fmac_f32_e32 v144, v101, v96
	v_cndmask_b32_e64 v145, v96, v144, s[10:11]
	v_cndmask_b32_e64 v145, v145, v140, s[8:9]
	v_fma_f32 v50, v102, v140, v143
	v_fmac_f32_e32 v50, v103, v96
	v_mfma_f32_16x16x4_f32 v[64:67], v92, v145, v[64:67]
	v_mfma_f32_16x16x4_f32 v[60:63], v93, v145, v[60:63]
	v_mfma_f32_16x16x4_f32 v[52:55], v94, v145, v[52:55]
	v_mfma_f32_16x16x4_f32 v[56:59], v95, v145, v[56:59]
	v_cndmask_b32_e64 v50, v50, v141, s[8:9]
	ds_write_b32 v3, v50 offset:0
	ds_read_b128 v[132:135], v0 offset:1024
	ds_read_b32 v97, v1 offset:512
	ds_read_b128 v[136:139], v2 offset:16
	v_cvt_pk_bf16_f32 v8, v64, v65
	v_cvt_pk_bf16_f32 v9, v66, v67
	v_cvt_pk_bf16_f32 v10, v60, v61
	v_cvt_pk_bf16_f32 v11, v62, v63
	v_cvt_pk_bf16_f32 v12, v52, v53
	v_cvt_pk_bf16_f32 v13, v54, v55
	s_waitcnt lgkmcnt(3)
	v_mfma_f32_16x16x32_bf16 v[140:143], v[104:107], v[8:11], 0
	v_cvt_pk_bf16_f32 v14, v56, v57
	v_cvt_pk_bf16_f32 v15, v58, v59
	v_pk_mul_f32 v[64:65], v[64:65], v[112:113]
	v_pk_mul_f32 v[66:67], v[66:67], v[114:115]
	v_mfma_f32_16x16x32_bf16 v[140:143], v[108:111], v[12:15], v[140:143]
	v_pk_mul_f32 v[60:61], v[60:61], v[116:117]
	v_pk_mul_f32 v[62:63], v[62:63], v[118:119]
	v_pk_mul_f32 v[52:53], v[52:53], v[120:121]
	v_pk_mul_f32 v[54:55], v[54:55], v[122:123]
	v_pk_mul_f32 v[56:57], v[56:57], v[128:129]
	v_pk_mul_f32 v[58:59], v[58:59], v[130:131]
	ds_read_b128 v[68:71], v98 offset:1024
	ds_read_b128 v[72:75], v98 offset:1088
	ds_read_b128 v[76:79], v99 offset:16896
	ds_read_b128 v[80:83], v99 offset:16960
	ds_read_b128 v[84:87], v99 offset:17024
	ds_read_b128 v[88:91], v99 offset:17088
	s_waitcnt lgkmcnt(6)
	v_fma_f32 v144, v136, v140, v142
	v_fmac_f32_e32 v144, v137, v97
	v_cndmask_b32_e64 v145, v97, v144, s[10:11]
	v_cndmask_b32_e64 v145, v145, v140, s[8:9]
	v_fma_f32 v50, v138, v140, v143
	v_fmac_f32_e32 v50, v139, v97
	v_mfma_f32_16x16x4_f32 v[64:67], v132, v145, v[64:67]
	v_mfma_f32_16x16x4_f32 v[60:63], v133, v145, v[60:63]
	v_mfma_f32_16x16x4_f32 v[52:55], v134, v145, v[52:55]
	v_mfma_f32_16x16x4_f32 v[56:59], v135, v145, v[56:59]
	v_cndmask_b32_e64 v50, v50, v141, s[8:9]
	ds_write_b32 v3, v50 offset:512
	ds_read_b128 v[92:95], v0 offset:2048
	ds_read_b32 v96, v1 offset:1024
	ds_read_b128 v[100:103], v2 offset:32
	v_cvt_pk_bf16_f32 v8, v64, v65
	v_cvt_pk_bf16_f32 v9, v66, v67
	v_cvt_pk_bf16_f32 v10, v60, v61
	v_cvt_pk_bf16_f32 v11, v62, v63
	v_cvt_pk_bf16_f32 v12, v52, v53
	v_cvt_pk_bf16_f32 v13, v54, v55
	s_waitcnt lgkmcnt(3)
	v_mfma_f32_16x16x32_bf16 v[140:143], v[68:71], v[8:11], 0
	v_cvt_pk_bf16_f32 v14, v56, v57
	v_cvt_pk_bf16_f32 v15, v58, v59
	v_pk_mul_f32 v[64:65], v[64:65], v[76:77]
	v_pk_mul_f32 v[66:67], v[66:67], v[78:79]
	v_mfma_f32_16x16x32_bf16 v[140:143], v[72:75], v[12:15], v[140:143]
	v_pk_mul_f32 v[60:61], v[60:61], v[80:81]
	v_pk_mul_f32 v[62:63], v[62:63], v[82:83]
	v_pk_mul_f32 v[52:53], v[52:53], v[84:85]
	v_pk_mul_f32 v[54:55], v[54:55], v[86:87]
	v_pk_mul_f32 v[56:57], v[56:57], v[88:89]
	v_pk_mul_f32 v[58:59], v[58:59], v[90:91]
	ds_read_b128 v[104:107], v98 offset:1536
	ds_read_b128 v[108:111], v98 offset:1600
	ds_read_b128 v[112:115], v99 offset:17152
	ds_read_b128 v[116:119], v99 offset:17216
	ds_read_b128 v[120:123], v99 offset:17280
	ds_read_b128 v[128:131], v99 offset:17344
	s_waitcnt lgkmcnt(6)
; __device__ __forceinline__ void scan_head(const Params& p, LAS unsigned char* lds, int bh, const int wave) {
;     ...
;             bf16x8 Pa0, Pa1, Qa0, Qa1; f32x4 Pw0, Pw1, Pw2, Pw3, Qw0, Qw1, Qw2, Qw3, Pcs, Qcs; float Pb0, Pb1, Pb2, Pb3, Pvt, Pvu, Qb0, Qb1, Qb2, Qb3, Qvt, Qvu;
;             SCAN_LD(P, 0);
; #pragma unroll 1
;             for (int pi = 0; pi < 16; pi += 2) {
;                 SCAN_LD(Q, pi + 1);
;                 SCAN_STEP(P, pi);
;                 if (pi + 2 < 16) SCAN_LD(P, pi + 2);
;                 SCAN_STEP(Q, pi + 1);
	v_fma_f32 v144, v100, v140, v142
	v_fmac_f32_e32 v144, v101, v96
	v_cndmask_b32_e64 v145, v96, v144, s[10:11]
	v_cndmask_b32_e64 v145, v145, v140, s[8:9]
	v_fma_f32 v50, v102, v140, v143
	v_fmac_f32_e32 v50, v103, v96
	v_mfma_f32_16x16x4_f32 v[64:67], v92, v145, v[64:67]
	v_mfma_f32_16x16x4_f32 v[60:63], v93, v145, v[60:63]
	v_mfma_f32_16x16x4_f32 v[52:55], v94, v145, v[52:55]
	v_mfma_f32_16x16x4_f32 v[56:59], v95, v145, v[56:59]
	v_cndmask_b32_e64 v50, v50, v141, s[8:9]
	ds_write_b32 v3, v50 offset:1024
	ds_read_b128 v[132:135], v0 offset:3072
	ds_read_b32 v97, v1 offset:1536
	ds_read_b128 v[136:139], v2 offset:48
	v_cvt_pk_bf16_f32 v8, v64, v65
	v_cvt_pk_bf16_f32 v9, v66, v67
	v_cvt_pk_bf16_f32 v10, v60, v61
	v_cvt_pk_bf16_f32 v11, v62, v63
	v_cvt_pk_bf16_f32 v12, v52, v53
	v_cvt_pk_bf16_f32 v13, v54, v55
	s_waitcnt lgkmcnt(3)
	v_mfma_f32_16x16x32_bf16 v[140:143], v[104:107], v[8:11], 0
	v_cvt_pk_bf16_f32 v14, v56, v57
	v_cvt_pk_bf16_f32 v15, v58, v59
	v_pk_mul_f32 v[64:65], v[64:65], v[112:113]
	v_pk_mul_f32 v[66:67], v[66:67], v[114:115]
	v_mfma_f32_16x16x32_bf16 v[140:143], v[108:111], v[12:15], v[140:143]
	v_pk_mul_f32 v[60:61], v[60:61], v[116:117]
	v_pk_mul_f32 v[62:63], v[62:63], v[118:119]
	v_pk_mul_f32 v[52:53], v[52:53], v[120:121]
	v_pk_mul_f32 v[54:55], v[54:55], v[122:123]
	v_pk_mul_f32 v[56:57], v[56:57], v[128:129]
	v_pk_mul_f32 v[58:59], v[58:59], v[130:131]
	ds_read_b128 v[68:71], v98 offset:2048
	ds_read_b128 v[72:75], v98 offset:2112
	ds_read_b128 v[76:79], v99 offset:17408
	ds_read_b128 v[80:83], v99 offset:17472
	ds_read_b128 v[84:87], v99 offset:17536
	ds_read_b128 v[88:91], v99 offset:17600
	s_waitcnt lgkmcnt(6)
	v_fma_f32 v144, v136, v140, v142
	v_fmac_f32_e32 v144, v137, v97
	v_cndmask_b32_e64 v145, v97, v144, s[10:11]
	v_cndmask_b32_e64 v145, v145, v140, s[8:9]
	v_fma_f32 v50, v138, v140, v143
	v_fmac_f32_e32 v50, v139, v97
	v_mfma_f32_16x16x4_f32 v[64:67], v132, v145, v[64:67]
	v_mfma_f32_16x16x4_f32 v[60:63], v133, v145, v[60:63]
	v_mfma_f32_16x16x4_f32 v[52:55], v134, v145, v[52:55]
	v_mfma_f32_16x16x4_f32 v[56:59], v135, v145, v[56:59]
	v_cndmask_b32_e64 v50, v50, v141, s[8:9]
	ds_write_b32 v3, v50 offset:1536
	ds_read_b128 v[92:95], v0 offset:4096
	ds_read_b32 v96, v1 offset:2048
	ds_read_b128 v[100:103], v2 offset:64
	v_cvt_pk_bf16_f32 v8, v64, v65
	v_cvt_pk_bf16_f32 v9, v66, v67
	v_cvt_pk_bf16_f32 v10, v60, v61
	v_cvt_pk_bf16_f32 v11, v62, v63
	v_cvt_pk_bf16_f32 v12, v52, v53
	v_cvt_pk_bf16_f32 v13, v54, v55
	s_waitcnt lgkmcnt(3)
	v_mfma_f32_16x16x32_bf16 v[140:143], v[68:71], v[8:11], 0
	v_cvt_pk_bf16_f32 v14, v56, v57
	v_cvt_pk_bf16_f32 v15, v58, v59
	v_pk_mul_f32 v[64:65], v[64:65], v[76:77]
	v_pk_mul_f32 v[66:67], v[66:67], v[78:79]
	v_mfma_f32_16x16x32_bf16 v[140:143], v[72:75], v[12:15], v[140:143]
	v_pk_mul_f32 v[60:61], v[60:61], v[80:81]
	v_pk_mul_f32 v[62:63], v[62:63], v[82:83]
	v_pk_mul_f32 v[52:53], v[52:53], v[84:85]
	v_pk_mul_f32 v[54:55], v[54:55], v[86:87]
	v_pk_mul_f32 v[56:57], v[56:57], v[88:89]
	v_pk_mul_f32 v[58:59], v[58:59], v[90:91]
	ds_read_b128 v[104:107], v98 offset:2560
	ds_read_b128 v[108:111], v98 offset:2624
	ds_read_b128 v[112:115], v99 offset:17664
	ds_read_b128 v[116:119], v99 offset:17728
	ds_read_b128 v[120:123], v99 offset:17792
	ds_read_b128 v[128:131], v99 offset:17856
	s_waitcnt lgkmcnt(6)
	v_fma_f32 v144, v100, v140, v142
	v_fmac_f32_e32 v144, v101, v96
	v_cndmask_b32_e64 v145, v96, v144, s[10:11]
	v_cndmask_b32_e64 v145, v145, v140, s[8:9]
	v_fma_f32 v50, v102, v140, v143
	v_fmac_f32_e32 v50, v103, v96
	v_mfma_f32_16x16x4_f32 v[64:67], v92, v145, v[64:67]
	v_mfma_f32_16x16x4_f32 v[60:63], v93, v145, v[60:63]
	v_mfma_f32_16x16x4_f32 v[52:55], v94, v145, v[52:55]
	v_mfma_f32_16x16x4_f32 v[56:59], v95, v145, v[56:59]
	v_cndmask_b32_e64 v50, v50, v141, s[8:9]
	ds_write_b32 v3, v50 offset:2048
	ds_read_b128 v[132:135], v0 offset:5120
	ds_read_b32 v97, v1 offset:2560
	ds_read_b128 v[136:139], v2 offset:80
	v_cvt_pk_bf16_f32 v8, v64, v65
	v_cvt_pk_bf16_f32 v9, v66, v67
	v_cvt_pk_bf16_f32 v10, v60, v61
	v_cvt_pk_bf16_f32 v11, v62, v63
	v_cvt_pk_bf16_f32 v12, v52, v53
	v_cvt_pk_bf16_f32 v13, v54, v55
	s_waitcnt lgkmcnt(3)
	v_mfma_f32_16x16x32_bf16 v[140:143], v[104:107], v[8:11], 0
	v_cvt_pk_bf16_f32 v14, v56, v57
	v_cvt_pk_bf16_f32 v15, v58, v59
	v_pk_mul_f32 v[64:65], v[64:65], v[112:113]
	v_pk_mul_f32 v[66:67], v[66:67], v[114:115]
	v_mfma_f32_16x16x32_bf16 v[140:143], v[108:111], v[12:15], v[140:143]
	v_pk_mul_f32 v[60:61], v[60:61], v[116:117]
	v_pk_mul_f32 v[62:63], v[62:63], v[118:119]
	v_pk_mul_f32 v[52:53], v[52:53], v[120:121]
	v_pk_mul_f32 v[54:55], v[54:55], v[122:123]
	v_pk_mul_f32 v[56:57], v[56:57], v[128:129]
	v_pk_mul_f32 v[58:59], v[58:59], v[130:131]
	ds_read_b128 v[68:71], v98 offset:3072
	ds_read_b128 v[72:75], v98 offset:3136
	ds_read_b128 v[76:79], v99 offset:17920
	ds_read_b128 v[80:83], v99 offset:17984
	ds_read_b128 v[84:87], v99 offset:18048
	ds_read_b128 v[88:91], v99 offset:18112
	s_waitcnt lgkmcnt(6)
	v_fma_f32 v144, v136, v140, v142
	v_fmac_f32_e32 v144, v137, v97
	v_cndmask_b32_e64 v145, v97, v144, s[10:11]
	v_cndmask_b32_e64 v145, v145, v140, s[8:9]
	v_fma_f32 v50, v138, v140, v143
	v_fmac_f32_e32 v50, v139, v97
	v_mfma_f32_16x16x4_f32 v[64:67], v132, v145, v[64:67]
	v_mfma_f32_16x16x4_f32 v[60:63], v133, v145, v[60:63]
	v_mfma_f32_16x16x4_f32 v[52:55], v134, v145, v[52:55]
	v_mfma_f32_16x16x4_f32 v[56:59], v135, v145, v[56:59]
	v_cndmask_b32_e64 v50, v50, v141, s[8:9]
	ds_write_b32 v3, v50 offset:2560
	ds_read_b128 v[92:95], v0 offset:6144
	ds_read_b32 v96, v1 offset:3072
	ds_read_b128 v[100:103], v2 offset:96
	v_cvt_pk_bf16_f32 v8, v64, v65
	v_cvt_pk_bf16_f32 v9, v66, v67
	v_cvt_pk_bf16_f32 v10, v60, v61
	v_cvt_pk_bf16_f32 v11, v62, v63
	v_cvt_pk_bf16_f32 v12, v52, v53
	v_cvt_pk_bf16_f32 v13, v54, v55
	s_waitcnt lgkmcnt(3)
; __device__ __forceinline__ void scan_head(const Params& p, LAS unsigned char* lds, int bh, const int wave) {
;     ...
;             bf16x8 Pa0, Pa1, Qa0, Qa1; f32x4 Pw0, Pw1, Pw2, Pw3, Qw0, Qw1, Qw2, Qw3, Pcs, Qcs; float Pb0, Pb1, Pb2, Pb3, Pvt, Pvu, Qb0, Qb1, Qb2, Qb3, Qvt, Qvu;
;             SCAN_LD(P, 0);
; #pragma unroll 1
;             for (int pi = 0; pi < 16; pi += 2) {
;                 SCAN_LD(Q, pi + 1);
;                 SCAN_STEP(P, pi);
;                 if (pi + 2 < 16) SCAN_LD(P, pi + 2);
;                 SCAN_STEP(Q, pi + 1);
	v_mfma_f32_16x16x32_bf16 v[140:143], v[68:71], v[8:11], 0
	v_cvt_pk_bf16_f32 v14, v56, v57
	v_cvt_pk_bf16_f32 v15, v58, v59
	v_pk_mul_f32 v[64:65], v[64:65], v[76:77]
	v_pk_mul_f32 v[66:67], v[66:67], v[78:79]
	v_mfma_f32_16x16x32_bf16 v[140:143], v[72:75], v[12:15], v[140:143]
	v_pk_mul_f32 v[60:61], v[60:61], v[80:81]
	v_pk_mul_f32 v[62:63], v[62:63], v[82:83]
	v_pk_mul_f32 v[52:53], v[52:53], v[84:85]
	v_pk_mul_f32 v[54:55], v[54:55], v[86:87]
	v_pk_mul_f32 v[56:57], v[56:57], v[88:89]
	v_pk_mul_f32 v[58:59], v[58:59], v[90:91]
	ds_read_b128 v[104:107], v98 offset:3584
	ds_read_b128 v[108:111], v98 offset:3648
	ds_read_b128 v[112:115], v99 offset:18176
	ds_read_b128 v[116:119], v99 offset:18240
	ds_read_b128 v[120:123], v99 offset:18304
	ds_read_b128 v[128:131], v99 offset:18368
	s_waitcnt lgkmcnt(6)
	v_fma_f32 v144, v100, v140, v142
	v_fmac_f32_e32 v144, v101, v96
	v_cndmask_b32_e64 v145, v96, v144, s[10:11]
	v_cndmask_b32_e64 v145, v145, v140, s[8:9]
	v_fma_f32 v50, v102, v140, v143
	v_fmac_f32_e32 v50, v103, v96
	v_mfma_f32_16x16x4_f32 v[64:67], v92, v145, v[64:67]
	v_mfma_f32_16x16x4_f32 v[60:63], v93, v145, v[60:63]
	v_mfma_f32_16x16x4_f32 v[52:55], v94, v145, v[52:55]
	v_mfma_f32_16x16x4_f32 v[56:59], v95, v145, v[56:59]
	v_cndmask_b32_e64 v50, v50, v141, s[8:9]
	ds_write_b32 v3, v50 offset:3072
	ds_read_b128 v[132:135], v0 offset:7168
	ds_read_b32 v97, v1 offset:3584
	ds_read_b128 v[136:139], v2 offset:112
	v_cvt_pk_bf16_f32 v8, v64, v65
	v_cvt_pk_bf16_f32 v9, v66, v67
	v_cvt_pk_bf16_f32 v10, v60, v61
	v_cvt_pk_bf16_f32 v11, v62, v63
	v_cvt_pk_bf16_f32 v12, v52, v53
	v_cvt_pk_bf16_f32 v13, v54, v55
	s_waitcnt lgkmcnt(3)
	v_mfma_f32_16x16x32_bf16 v[140:143], v[104:107], v[8:11], 0
	v_cvt_pk_bf16_f32 v14, v56, v57
	v_cvt_pk_bf16_f32 v15, v58, v59
	v_pk_mul_f32 v[64:65], v[64:65], v[112:113]
	v_pk_mul_f32 v[66:67], v[66:67], v[114:115]
	v_mfma_f32_16x16x32_bf16 v[140:143], v[108:111], v[12:15], v[140:143]
	v_pk_mul_f32 v[60:61], v[60:61], v[116:117]
	v_pk_mul_f32 v[62:63], v[62:63], v[118:119]
	v_pk_mul_f32 v[52:53], v[52:53], v[120:121]
	v_pk_mul_f32 v[54:55], v[54:55], v[122:123]
	v_pk_mul_f32 v[56:57], v[56:57], v[128:129]
	v_pk_mul_f32 v[58:59], v[58:59], v[130:131]
	ds_read_b128 v[68:71], v98 offset:4096
	ds_read_b128 v[72:75], v98 offset:4160
	ds_read_b128 v[76:79], v99 offset:18432
	ds_read_b128 v[80:83], v99 offset:18496
	ds_read_b128 v[84:87], v99 offset:18560
	ds_read_b128 v[88:91], v99 offset:18624
	s_waitcnt lgkmcnt(6)
	v_fma_f32 v144, v136, v140, v142
	v_fmac_f32_e32 v144, v137, v97
	v_cndmask_b32_e64 v145, v97, v144, s[10:11]
	v_cndmask_b32_e64 v145, v145, v140, s[8:9]
	v_fma_f32 v50, v138, v140, v143
	v_fmac_f32_e32 v50, v139, v97
	v_mfma_f32_16x16x4_f32 v[64:67], v132, v145, v[64:67]
	v_mfma_f32_16x16x4_f32 v[60:63], v133, v145, v[60:63]
	v_mfma_f32_16x16x4_f32 v[52:55], v134, v145, v[52:55]
	v_mfma_f32_16x16x4_f32 v[56:59], v135, v145, v[56:59]
	v_cndmask_b32_e64 v50, v50, v141, s[8:9]
	ds_write_b32 v3, v50 offset:3584
	ds_read_b128 v[92:95], v0 offset:8192
	ds_read_b32 v96, v1 offset:4096
	ds_read_b128 v[100:103], v2 offset:128
	v_cvt_pk_bf16_f32 v8, v64, v65
	v_cvt_pk_bf16_f32 v9, v66, v67
	v_cvt_pk_bf16_f32 v10, v60, v61
	v_cvt_pk_bf16_f32 v11, v62, v63
	v_cvt_pk_bf16_f32 v12, v52, v53
	v_cvt_pk_bf16_f32 v13, v54, v55
	s_waitcnt lgkmcnt(3)
	v_mfma_f32_16x16x32_bf16 v[140:143], v[68:71], v[8:11], 0
	v_cvt_pk_bf16_f32 v14, v56, v57
	v_cvt_pk_bf16_f32 v15, v58, v59
	v_pk_mul_f32 v[64:65], v[64:65], v[76:77]
	v_pk_mul_f32 v[66:67], v[66:67], v[78:79]
	v_mfma_f32_16x16x32_bf16 v[140:143], v[72:75], v[12:15], v[140:143]
	v_pk_mul_f32 v[60:61], v[60:61], v[80:81]
	v_pk_mul_f32 v[62:63], v[62:63], v[82:83]
	v_pk_mul_f32 v[52:53], v[52:53], v[84:85]
	v_pk_mul_f32 v[54:55], v[54:55], v[86:87]
	v_pk_mul_f32 v[56:57], v[56:57], v[88:89]
	v_pk_mul_f32 v[58:59], v[58:59], v[90:91]
	ds_read_b128 v[104:107], v98 offset:4608
	ds_read_b128 v[108:111], v98 offset:4672
	ds_read_b128 v[112:115], v99 offset:18688
	ds_read_b128 v[116:119], v99 offset:18752
	ds_read_b128 v[120:123], v99 offset:18816
	ds_read_b128 v[128:131], v99 offset:18880
	s_waitcnt lgkmcnt(6)
	v_fma_f32 v144, v100, v140, v142
	v_fmac_f32_e32 v144, v101, v96
	v_cndmask_b32_e64 v145, v96, v144, s[10:11]
	v_cndmask_b32_e64 v145, v145, v140, s[8:9]
	v_fma_f32 v50, v102, v140, v143
	v_fmac_f32_e32 v50, v103, v96
	v_mfma_f32_16x16x4_f32 v[64:67], v92, v145, v[64:67]
	v_mfma_f32_16x16x4_f32 v[60:63], v93, v145, v[60:63]
	v_mfma_f32_16x16x4_f32 v[52:55], v94, v145, v[52:55]
	v_mfma_f32_16x16x4_f32 v[56:59], v95, v145, v[56:59]
	v_cndmask_b32_e64 v50, v50, v141, s[8:9]
	ds_write_b32 v3, v50 offset:4096
	ds_read_b128 v[132:135], v0 offset:9216
	ds_read_b32 v97, v1 offset:4608
	ds_read_b128 v[136:139], v2 offset:144
	v_cvt_pk_bf16_f32 v8, v64, v65
	v_cvt_pk_bf16_f32 v9, v66, v67
	v_cvt_pk_bf16_f32 v10, v60, v61
	v_cvt_pk_bf16_f32 v11, v62, v63
	v_cvt_pk_bf16_f32 v12, v52, v53
	v_cvt_pk_bf16_f32 v13, v54, v55
	s_waitcnt lgkmcnt(3)
	v_mfma_f32_16x16x32_bf16 v[140:143], v[104:107], v[8:11], 0
	v_cvt_pk_bf16_f32 v14, v56, v57
	v_cvt_pk_bf16_f32 v15, v58, v59
	v_pk_mul_f32 v[64:65], v[64:65], v[112:113]
	v_pk_mul_f32 v[66:67], v[66:67], v[114:115]
	v_mfma_f32_16x16x32_bf16 v[140:143], v[108:111], v[12:15], v[140:143]
	v_pk_mul_f32 v[60:61], v[60:61], v[116:117]
	v_pk_mul_f32 v[62:63], v[62:63], v[118:119]
	v_pk_mul_f32 v[52:53], v[52:53], v[120:121]
	v_pk_mul_f32 v[54:55], v[54:55], v[122:123]
	v_pk_mul_f32 v[56:57], v[56:57], v[128:129]
	v_pk_mul_f32 v[58:59], v[58:59], v[130:131]
	ds_read_b128 v[68:71], v98 offset:5120
	ds_read_b128 v[72:75], v98 offset:5184
	ds_read_b128 v[76:79], v99 offset:18944
	ds_read_b128 v[80:83], v99 offset:19008
	ds_read_b128 v[84:87], v99 offset:19072
	ds_read_b128 v[88:91], v99 offset:19136
	s_waitcnt lgkmcnt(6)
; __device__ __forceinline__ void scan_head(const Params& p, LAS unsigned char* lds, int bh, const int wave) {
;     ...
;             bf16x8 Pa0, Pa1, Qa0, Qa1; f32x4 Pw0, Pw1, Pw2, Pw3, Qw0, Qw1, Qw2, Qw3, Pcs, Qcs; float Pb0, Pb1, Pb2, Pb3, Pvt, Pvu, Qb0, Qb1, Qb2, Qb3, Qvt, Qvu;
;             SCAN_LD(P, 0);
; #pragma unroll 1
;             for (int pi = 0; pi < 16; pi += 2) {
;                 SCAN_LD(Q, pi + 1);
;                 SCAN_STEP(P, pi);
;                 if (pi + 2 < 16) SCAN_LD(P, pi + 2);
;                 SCAN_STEP(Q, pi + 1);
	v_fma_f32 v144, v136, v140, v142
	v_fmac_f32_e32 v144, v137, v97
	v_cndmask_b32_e64 v145, v97, v144, s[10:11]
	v_cndmask_b32_e64 v145, v145, v140, s[8:9]
	v_fma_f32 v50, v138, v140, v143
	v_fmac_f32_e32 v50, v139, v97
	v_mfma_f32_16x16x4_f32 v[64:67], v132, v145, v[64:67]
	v_mfma_f32_16x16x4_f32 v[60:63], v133, v145, v[60:63]
	v_mfma_f32_16x16x4_f32 v[52:55], v134, v145, v[52:55]
	v_mfma_f32_16x16x4_f32 v[56:59], v135, v145, v[56:59]
	v_cndmask_b32_e64 v50, v50, v141, s[8:9]
	ds_write_b32 v3, v50 offset:4608
	ds_read_b128 v[92:95], v0 offset:10240
	ds_read_b32 v96, v1 offset:5120
	ds_read_b128 v[100:103], v2 offset:160
	v_cvt_pk_bf16_f32 v8, v64, v65
	v_cvt_pk_bf16_f32 v9, v66, v67
	v_cvt_pk_bf16_f32 v10, v60, v61
	v_cvt_pk_bf16_f32 v11, v62, v63
	v_cvt_pk_bf16_f32 v12, v52, v53
	v_cvt_pk_bf16_f32 v13, v54, v55
	s_waitcnt lgkmcnt(3)
	v_mfma_f32_16x16x32_bf16 v[140:143], v[68:71], v[8:11], 0
	v_cvt_pk_bf16_f32 v14, v56, v57
	v_cvt_pk_bf16_f32 v15, v58, v59
	v_pk_mul_f32 v[64:65], v[64:65], v[76:77]
	v_pk_mul_f32 v[66:67], v[66:67], v[78:79]
	v_mfma_f32_16x16x32_bf16 v[140:143], v[72:75], v[12:15], v[140:143]
	v_pk_mul_f32 v[60:61], v[60:61], v[80:81]
	v_pk_mul_f32 v[62:63], v[62:63], v[82:83]
	v_pk_mul_f32 v[52:53], v[52:53], v[84:85]
	v_pk_mul_f32 v[54:55], v[54:55], v[86:87]
	v_pk_mul_f32 v[56:57], v[56:57], v[88:89]
	v_pk_mul_f32 v[58:59], v[58:59], v[90:91]
	ds_read_b128 v[104:107], v98 offset:5632
	ds_read_b128 v[108:111], v98 offset:5696
	ds_read_b128 v[112:115], v99 offset:19200
	ds_read_b128 v[116:119], v99 offset:19264
	ds_read_b128 v[120:123], v99 offset:19328
	ds_read_b128 v[128:131], v99 offset:19392
	s_waitcnt lgkmcnt(6)
	v_fma_f32 v144, v100, v140, v142
	v_fmac_f32_e32 v144, v101, v96
	v_cndmask_b32_e64 v145, v96, v144, s[10:11]
	v_cndmask_b32_e64 v145, v145, v140, s[8:9]
	v_fma_f32 v50, v102, v140, v143
	v_fmac_f32_e32 v50, v103, v96
	v_mfma_f32_16x16x4_f32 v[64:67], v92, v145, v[64:67]
	v_mfma_f32_16x16x4_f32 v[60:63], v93, v145, v[60:63]
	v_mfma_f32_16x16x4_f32 v[52:55], v94, v145, v[52:55]
	v_mfma_f32_16x16x4_f32 v[56:59], v95, v145, v[56:59]
	v_cndmask_b32_e64 v50, v50, v141, s[8:9]
	ds_write_b32 v3, v50 offset:5120
	ds_read_b128 v[132:135], v0 offset:11264
	ds_read_b32 v97, v1 offset:5632
	ds_read_b128 v[136:139], v2 offset:176
	v_cvt_pk_bf16_f32 v8, v64, v65
	v_cvt_pk_bf16_f32 v9, v66, v67
	v_cvt_pk_bf16_f32 v10, v60, v61
	v_cvt_pk_bf16_f32 v11, v62, v63
	v_cvt_pk_bf16_f32 v12, v52, v53
	v_cvt_pk_bf16_f32 v13, v54, v55
	s_waitcnt lgkmcnt(3)
	v_mfma_f32_16x16x32_bf16 v[140:143], v[104:107], v[8:11], 0
	v_cvt_pk_bf16_f32 v14, v56, v57
	v_cvt_pk_bf16_f32 v15, v58, v59
	v_pk_mul_f32 v[64:65], v[64:65], v[112:113]
	v_pk_mul_f32 v[66:67], v[66:67], v[114:115]
	v_mfma_f32_16x16x32_bf16 v[140:143], v[108:111], v[12:15], v[140:143]
	v_pk_mul_f32 v[60:61], v[60:61], v[116:117]
	v_pk_mul_f32 v[62:63], v[62:63], v[118:119]
	v_pk_mul_f32 v[52:53], v[52:53], v[120:121]
	v_pk_mul_f32 v[54:55], v[54:55], v[122:123]
	v_pk_mul_f32 v[56:57], v[56:57], v[128:129]
	v_pk_mul_f32 v[58:59], v[58:59], v[130:131]
	ds_read_b128 v[68:71], v98 offset:6144
	ds_read_b128 v[72:75], v98 offset:6208
	ds_read_b128 v[76:79], v99 offset:19456
	ds_read_b128 v[80:83], v99 offset:19520
	ds_read_b128 v[84:87], v99 offset:19584
	ds_read_b128 v[88:91], v99 offset:19648
	s_waitcnt lgkmcnt(6)
	v_fma_f32 v144, v136, v140, v142
	v_fmac_f32_e32 v144, v137, v97
	v_cndmask_b32_e64 v145, v97, v144, s[10:11]
	v_cndmask_b32_e64 v145, v145, v140, s[8:9]
	v_fma_f32 v50, v138, v140, v143
	v_fmac_f32_e32 v50, v139, v97
	v_mfma_f32_16x16x4_f32 v[64:67], v132, v145, v[64:67]
	v_mfma_f32_16x16x4_f32 v[60:63], v133, v145, v[60:63]
	v_mfma_f32_16x16x4_f32 v[52:55], v134, v145, v[52:55]
	v_mfma_f32_16x16x4_f32 v[56:59], v135, v145, v[56:59]
	v_cndmask_b32_e64 v50, v50, v141, s[8:9]
	ds_write_b32 v3, v50 offset:5632
	ds_read_b128 v[92:95], v0 offset:12288
	ds_read_b32 v96, v1 offset:6144
	ds_read_b128 v[100:103], v2 offset:192
	v_cvt_pk_bf16_f32 v8, v64, v65
	v_cvt_pk_bf16_f32 v9, v66, v67
	v_cvt_pk_bf16_f32 v10, v60, v61
	v_cvt_pk_bf16_f32 v11, v62, v63
	v_cvt_pk_bf16_f32 v12, v52, v53
	v_cvt_pk_bf16_f32 v13, v54, v55
	s_waitcnt lgkmcnt(3)
	v_mfma_f32_16x16x32_bf16 v[140:143], v[68:71], v[8:11], 0
	v_cvt_pk_bf16_f32 v14, v56, v57
	v_cvt_pk_bf16_f32 v15, v58, v59
	v_pk_mul_f32 v[64:65], v[64:65], v[76:77]
	v_pk_mul_f32 v[66:67], v[66:67], v[78:79]
	v_mfma_f32_16x16x32_bf16 v[140:143], v[72:75], v[12:15], v[140:143]
	v_pk_mul_f32 v[60:61], v[60:61], v[80:81]
	v_pk_mul_f32 v[62:63], v[62:63], v[82:83]
	v_pk_mul_f32 v[52:53], v[52:53], v[84:85]
	v_pk_mul_f32 v[54:55], v[54:55], v[86:87]
	v_pk_mul_f32 v[56:57], v[56:57], v[88:89]
	v_pk_mul_f32 v[58:59], v[58:59], v[90:91]
	ds_read_b128 v[104:107], v98 offset:6656
	ds_read_b128 v[108:111], v98 offset:6720
	ds_read_b128 v[112:115], v99 offset:19712
	ds_read_b128 v[116:119], v99 offset:19776
	ds_read_b128 v[120:123], v99 offset:19840
	ds_read_b128 v[128:131], v99 offset:19904
	s_waitcnt lgkmcnt(6)
; __device__ __forceinline__ void scan_head(const Params& p, LAS unsigned char* lds, int bh, const int wave) {
;     ...
;             bf16x8 Pa0, Pa1, Qa0, Qa1; f32x4 Pw0, Pw1, Pw2, Pw3, Qw0, Qw1, Qw2, Qw3, Pcs, Qcs; float Pb0, Pb1, Pb2, Pb3, Pvt, Pvu, Qb0, Qb1, Qb2, Qb3, Qvt, Qvu;
;             SCAN_LD(P, 0);
; #pragma unroll 1
;             for (int pi = 0; pi < 16; pi += 2) {
;                 SCAN_LD(Q, pi + 1);
;                 SCAN_STEP(P, pi);
;                 if (pi + 2 < 16) SCAN_LD(P, pi + 2);
;                 SCAN_STEP(Q, pi + 1);
;             }
	v_fma_f32 v144, v100, v140, v142
	v_fmac_f32_e32 v144, v101, v96
	v_cndmask_b32_e64 v145, v96, v144, s[10:11]
	v_cndmask_b32_e64 v145, v145, v140, s[8:9]
	v_fma_f32 v50, v102, v140, v143
	v_fmac_f32_e32 v50, v103, v96
	v_mfma_f32_16x16x4_f32 v[64:67], v92, v145, v[64:67]
	v_mfma_f32_16x16x4_f32 v[60:63], v93, v145, v[60:63]
	v_mfma_f32_16x16x4_f32 v[52:55], v94, v145, v[52:55]
	v_mfma_f32_16x16x4_f32 v[56:59], v95, v145, v[56:59]
	v_cndmask_b32_e64 v50, v50, v141, s[8:9]
	ds_write_b32 v3, v50 offset:6144
	ds_read_b128 v[132:135], v0 offset:13312
	ds_read_b32 v97, v1 offset:6656
	ds_read_b128 v[136:139], v2 offset:208
	v_cvt_pk_bf16_f32 v8, v64, v65
	v_cvt_pk_bf16_f32 v9, v66, v67
	v_cvt_pk_bf16_f32 v10, v60, v61
	v_cvt_pk_bf16_f32 v11, v62, v63
	v_cvt_pk_bf16_f32 v12, v52, v53
	v_cvt_pk_bf16_f32 v13, v54, v55
	s_waitcnt lgkmcnt(3)
	v_mfma_f32_16x16x32_bf16 v[140:143], v[104:107], v[8:11], 0
	v_cvt_pk_bf16_f32 v14, v56, v57
	v_cvt_pk_bf16_f32 v15, v58, v59
	v_pk_mul_f32 v[64:65], v[64:65], v[112:113]
	v_pk_mul_f32 v[66:67], v[66:67], v[114:115]
	v_mfma_f32_16x16x32_bf16 v[140:143], v[108:111], v[12:15], v[140:143]
	v_pk_mul_f32 v[60:61], v[60:61], v[116:117]
	v_pk_mul_f32 v[62:63], v[62:63], v[118:119]
	v_pk_mul_f32 v[52:53], v[52:53], v[120:121]
	v_pk_mul_f32 v[54:55], v[54:55], v[122:123]
	v_pk_mul_f32 v[56:57], v[56:57], v[128:129]
	v_pk_mul_f32 v[58:59], v[58:59], v[130:131]
	ds_read_b128 v[68:71], v98 offset:7168
	ds_read_b128 v[72:75], v98 offset:7232
	ds_read_b128 v[76:79], v99 offset:19968
	ds_read_b128 v[80:83], v99 offset:20032
	ds_read_b128 v[84:87], v99 offset:20096
	ds_read_b128 v[88:91], v99 offset:20160
	s_waitcnt lgkmcnt(6)
	v_fma_f32 v144, v136, v140, v142
	v_fmac_f32_e32 v144, v137, v97
	v_cndmask_b32_e64 v145, v97, v144, s[10:11]
	v_cndmask_b32_e64 v145, v145, v140, s[8:9]
	v_fma_f32 v50, v138, v140, v143
	v_fmac_f32_e32 v50, v139, v97
	v_mfma_f32_16x16x4_f32 v[64:67], v132, v145, v[64:67]
	v_mfma_f32_16x16x4_f32 v[60:63], v133, v145, v[60:63]
	v_mfma_f32_16x16x4_f32 v[52:55], v134, v145, v[52:55]
	v_mfma_f32_16x16x4_f32 v[56:59], v135, v145, v[56:59]
	v_cndmask_b32_e64 v50, v50, v141, s[8:9]
	ds_write_b32 v3, v50 offset:6656
	ds_read_b128 v[92:95], v0 offset:14336
	ds_read_b32 v96, v1 offset:7168
	ds_read_b128 v[100:103], v2 offset:224
	v_cvt_pk_bf16_f32 v8, v64, v65
	v_cvt_pk_bf16_f32 v9, v66, v67
	v_cvt_pk_bf16_f32 v10, v60, v61
	v_cvt_pk_bf16_f32 v11, v62, v63
	v_cvt_pk_bf16_f32 v12, v52, v53
	v_cvt_pk_bf16_f32 v13, v54, v55
	s_waitcnt lgkmcnt(3)
	v_mfma_f32_16x16x32_bf16 v[140:143], v[68:71], v[8:11], 0
	v_cvt_pk_bf16_f32 v14, v56, v57
	v_cvt_pk_bf16_f32 v15, v58, v59
	v_pk_mul_f32 v[64:65], v[64:65], v[76:77]
	v_pk_mul_f32 v[66:67], v[66:67], v[78:79]
	v_mfma_f32_16x16x32_bf16 v[140:143], v[72:75], v[12:15], v[140:143]
	v_pk_mul_f32 v[60:61], v[60:61], v[80:81]
	v_pk_mul_f32 v[62:63], v[62:63], v[82:83]
	v_pk_mul_f32 v[52:53], v[52:53], v[84:85]
	v_pk_mul_f32 v[54:55], v[54:55], v[86:87]
	v_pk_mul_f32 v[56:57], v[56:57], v[88:89]
	v_pk_mul_f32 v[58:59], v[58:59], v[90:91]
	ds_read_b128 v[104:107], v98 offset:7680
	ds_read_b128 v[108:111], v98 offset:7744
	ds_read_b128 v[112:115], v99 offset:20224
	ds_read_b128 v[116:119], v99 offset:20288
	ds_read_b128 v[120:123], v99 offset:20352
	ds_read_b128 v[128:131], v99 offset:20416
	s_waitcnt lgkmcnt(6)
	v_fma_f32 v144, v100, v140, v142
	v_fmac_f32_e32 v144, v101, v96
	v_cndmask_b32_e64 v145, v96, v144, s[10:11]
	v_cndmask_b32_e64 v145, v145, v140, s[8:9]
	v_fma_f32 v50, v102, v140, v143
	v_fmac_f32_e32 v50, v103, v96
	v_mfma_f32_16x16x4_f32 v[64:67], v92, v145, v[64:67]
	v_mfma_f32_16x16x4_f32 v[60:63], v93, v145, v[60:63]
	v_mfma_f32_16x16x4_f32 v[52:55], v94, v145, v[52:55]
	v_mfma_f32_16x16x4_f32 v[56:59], v95, v145, v[56:59]
	v_cndmask_b32_e64 v50, v50, v141, s[8:9]
	ds_write_b32 v3, v50 offset:7168
	ds_read_b128 v[132:135], v0 offset:15360
	ds_read_b32 v97, v1 offset:7680
	ds_read_b128 v[136:139], v2 offset:240
	v_cvt_pk_bf16_f32 v8, v64, v65
	v_cvt_pk_bf16_f32 v9, v66, v67
	v_cvt_pk_bf16_f32 v10, v60, v61
	v_cvt_pk_bf16_f32 v11, v62, v63
	v_cvt_pk_bf16_f32 v12, v52, v53
	v_cvt_pk_bf16_f32 v13, v54, v55
	s_waitcnt lgkmcnt(3)
	v_mfma_f32_16x16x32_bf16 v[140:143], v[104:107], v[8:11], 0
	v_cvt_pk_bf16_f32 v14, v56, v57
	v_cvt_pk_bf16_f32 v15, v58, v59
	v_pk_mul_f32 v[64:65], v[64:65], v[112:113]
	v_pk_mul_f32 v[66:67], v[66:67], v[114:115]
	v_mfma_f32_16x16x32_bf16 v[140:143], v[108:111], v[12:15], v[140:143]
	v_pk_mul_f32 v[60:61], v[60:61], v[116:117]
	v_pk_mul_f32 v[62:63], v[62:63], v[118:119]
	v_pk_mul_f32 v[52:53], v[52:53], v[120:121]
	v_pk_mul_f32 v[54:55], v[54:55], v[122:123]
	v_pk_mul_f32 v[56:57], v[56:57], v[128:129]
	v_pk_mul_f32 v[58:59], v[58:59], v[130:131]
	s_waitcnt lgkmcnt(0)
	s_nop 1
	v_fma_f32 v144, v136, v140, v142
	v_fmac_f32_e32 v144, v137, v97
	v_cndmask_b32_e64 v145, v97, v144, s[10:11]
	v_cndmask_b32_e64 v145, v145, v140, s[8:9]
	v_fma_f32 v50, v138, v140, v143
	v_fmac_f32_e32 v50, v139, v97
	v_mfma_f32_16x16x4_f32 v[64:67], v132, v145, v[64:67]
	v_mfma_f32_16x16x4_f32 v[60:63], v133, v145, v[60:63]
	v_mfma_f32_16x16x4_f32 v[52:55], v134, v145, v[52:55]
	v_mfma_f32_16x16x4_f32 v[56:59], v135, v145, v[56:59]
	v_cndmask_b32_e64 v50, v50, v141, s[8:9]
	ds_write_b32 v3, v50 offset:7680
	s_nop 7
